# v14 + P9 stage A: first gather batch of the next slice requested during the last token's reduction (fresh registers, copied into place at the next slice's top)
# baseline (speedup 1.0000x reference)
; #define P9A_LOAD(W, J, H) do { _Pragma("unroll") for (int i = 0; i < 8; ++i) { const unsigned e = IDX16[(F.wave * 8 + (J)) * 128 + 64 * (H) + 8 * g + i]; W[i] = *(const GAS v4u*)(eb + (e * 2048u + lo)); } } while (0)
; DI void p9v2_phase(Frame& F) {
;     ...
;         if (tid < 64) SH[tid] = F.SA[tb + tid];
;         __syncthreads();
; #pragma unroll
;         for (int i = 0; i < 16; ++i) { const int q = tid + 512 * i, k = q & 127; IDX16[(q & ~127) + (k & 64) + 8 * (k & 7) + ((k >> 3) & 7)] = (unsigned short)F.IDX[(size_t)tb * NSEL + q]; }
;         __syncthreads();
;         int P[8][2];
; #pragma unroll
;         for (int j = 0; j < 8; ++j) { P[j][0] = 0; P[j][1] = 0; }
; #pragma unroll 1
;         for (int s = 0; s < NSLICE_A; ++s) {
;             if (((s ^ (F.wave >> 2)) & 1) != 0) __builtin_amdgcn_s_setprio(1); else __builtin_amdgcn_s_setprio(0);
;             const unsigned char* eb = F.ED + s * SLICE_B;
;             const unsigned lo = (unsigned)(c8 * 16);
;             v4u wA[8], wB[8];
;     ...
;             P9A_LOAD(wA, 0, 0);
.LBB0_1301:
	s_or_b64 exec, exec, s[44:45]
	s_ashr_i32 s23, s22, 31
	s_lshl_b64 s[44:45], s[22:23], 9
	s_add_u32 s44, s16, s44
	s_addc_u32 s45, s17, s45
	v_lshl_add_u64 v[2:3], s[44:45], 0, v[146:147]
	v_add_co_u32_e32 v4, vcc, s27, v2
	s_waitcnt lgkmcnt(0)
	s_nop 0
	v_addc_co_u32_e32 v5, vcc, 0, v3, vcc
	v_add_co_u32_e32 v6, vcc, s68, v2
	s_barrier
	s_nop 0
	v_addc_co_u32_e32 v7, vcc, 0, v3, vcc
	v_add_co_u32_e32 v8, vcc, s69, v2
	s_nop 1
	v_addc_co_u32_e32 v9, vcc, 0, v3, vcc
	v_add_co_u32_e32 v10, vcc, s70, v2
	global_load_dword v19, v146, s[44:45]
	global_load_dword v20, v146, s[44:45] offset:2048
	v_addc_co_u32_e32 v11, vcc, 0, v3, vcc
	global_load_dword v21, v188, s[44:45]
	global_load_dword v22, v[4:5], off offset:2048
	global_load_dword v23, v189, s[44:45]
	global_load_dword v24, v[6:7], off offset:2048
	global_load_dword v25, v190, s[44:45]
	global_load_dword v26, v[8:9], off offset:2048
	global_load_dword v27, v191, s[44:45]
	global_load_dword v28, v[10:11], off offset:2048
	v_add_co_u32_e32 v4, vcc, s71, v2
	s_mov_b32 s23, 0
	s_nop 0
	v_addc_co_u32_e32 v5, vcc, 0, v3, vcc
	v_add_co_u32_e32 v6, vcc, s72, v2
	v_mov_b32_e32 v8, 0
	s_nop 0
	v_addc_co_u32_e32 v7, vcc, 0, v3, vcc
	v_add_co_u32_e32 v2, vcc, 0x7000, v2
	v_mov_b32_e32 v9, 0
	s_nop 0
	v_addc_co_u32_e32 v3, vcc, 0, v3, vcc
	global_load_dword v29, v192, s[44:45]
	s_nop 0
	global_load_dword v4, v[4:5], off offset:2048
	s_nop 0
	global_load_dword v5, v193, s[44:45]
	global_load_dword v30, v[6:7], off offset:2048
	global_load_dword v31, v194, s[44:45]
	s_nop 0
	global_load_dword v3, v[2:3], off offset:2048
	v_mov_b32_e32 v6, 0
	s_mov_b64 s[44:45], 0
	v_mov_b32_e32 v2, v182
	v_mov_b32_e32 v7, 0
	v_mov_b32_e32 v10, 0
	v_mov_b32_e32 v11, 0
	v_mov_b32_e32 v12, 0
	v_mov_b32_e32 v13, 0
	v_mov_b32_e32 v14, 0
	v_mov_b32_e32 v15, 0
	v_mov_b32_e32 v16, 0
	v_mov_b32_e32 v17, 0
	v_mov_b32_e32 v18, 0
	s_waitcnt vmcnt(15)
	ds_write_b16 v164, v19
	s_waitcnt vmcnt(14)
	ds_write_b16 v165, v20
	s_waitcnt vmcnt(13)
	ds_write_b16 v166, v21
	s_waitcnt vmcnt(12)
	ds_write_b16 v167, v22
	s_waitcnt vmcnt(11)
	ds_write_b16 v168, v23
	s_waitcnt vmcnt(10)
	ds_write_b16 v169, v24
	s_waitcnt vmcnt(9)
	ds_write_b16 v170, v25
	s_waitcnt vmcnt(8)
	ds_write_b16 v171, v26
	s_waitcnt vmcnt(7)
	ds_write_b16 v172, v27
	s_waitcnt vmcnt(6)
	ds_write_b16 v173, v28
	s_waitcnt vmcnt(5)
	ds_write_b16 v174, v29
	s_waitcnt vmcnt(4)
	ds_write_b16 v175, v4
	s_waitcnt vmcnt(3)
	ds_write_b16 v176, v5
	s_waitcnt vmcnt(2)
	ds_write_b16 v177, v30
	s_waitcnt vmcnt(1)
	ds_write_b16 v178, v31
	s_waitcnt vmcnt(0)
	ds_write_b16 v179, v3
	v_mov_b32_e32 v19, 0
	v_mov_b32_e32 v20, 0
	v_mov_b32_e32 v21, 0
	s_waitcnt lgkmcnt(0)
	s_barrier
	s_add_u32 s84, s37, s44
	s_addc_u32 s85, s39, s45
	ds_read_b128 v[216:219], v195
	s_waitcnt lgkmcnt(0)
	v_lshlrev_b32_sdwa v214, v198, v216 dst_sel:DWORD dst_unused:UNUSED_PAD src0_sel:DWORD src1_sel:WORD_0
	v_lshlrev_b32_sdwa v215, v198, v216 dst_sel:DWORD dst_unused:UNUSED_PAD src0_sel:DWORD src1_sel:WORD_1
	v_or_b32_e32 v214, v214, v130
	v_or_b32_e32 v215, v215, v1
	global_load_dwordx4 v[220:223], v214, s[84:85]
	global_load_dwordx4 v[224:227], v215, s[84:85]
	v_lshlrev_b32_sdwa v214, v198, v217 dst_sel:DWORD dst_unused:UNUSED_PAD src0_sel:DWORD src1_sel:WORD_0
	v_lshlrev_b32_sdwa v215, v198, v217 dst_sel:DWORD dst_unused:UNUSED_PAD src0_sel:DWORD src1_sel:WORD_1
	v_or_b32_e32 v214, v214, v130
	v_or_b32_e32 v215, v215, v1
	global_load_dwordx4 v[228:231], v214, s[84:85]
	global_load_dwordx4 v[232:235], v215, s[84:85]
	v_lshlrev_b32_sdwa v214, v198, v218 dst_sel:DWORD dst_unused:UNUSED_PAD src0_sel:DWORD src1_sel:WORD_0
	v_lshlrev_b32_sdwa v215, v198, v218 dst_sel:DWORD dst_unused:UNUSED_PAD src0_sel:DWORD src1_sel:WORD_1
	v_or_b32_e32 v214, v214, v130
	v_or_b32_e32 v215, v215, v1
	global_load_dwordx4 v[236:239], v214, s[84:85]
	global_load_dwordx4 v[240:243], v215, s[84:85]
	v_lshlrev_b32_sdwa v214, v198, v219 dst_sel:DWORD dst_unused:UNUSED_PAD src0_sel:DWORD src1_sel:WORD_0
	v_lshlrev_b32_sdwa v215, v198, v219 dst_sel:DWORD dst_unused:UNUSED_PAD src0_sel:DWORD src1_sel:WORD_1
	v_or_b32_e32 v214, v214, v130
	v_or_b32_e32 v215, v215, v1
	global_load_dwordx4 v[244:247], v214, s[84:85]
	global_load_dwordx4 v[248:251], v215, s[84:85]
	s_branch .LBB0_1303
; #define P9A_LOAD(W, J, H) do { _Pragma("unroll") for (int i = 0; i < 8; ++i) { const unsigned e = IDX16[(F.wave * 8 + (J)) * 128 + 64 * (H) + 8 * g + i]; W[i] = *(const GAS v4u*)(eb + (e * 2048u + lo)); } } while (0)
; DI void p9v2_phase(Frame& F) {
;     ...
;         for (int s = 0; s < NSLICE_A; ++s) {
;             if (((s ^ (F.wave >> 2)) & 1) != 0) __builtin_amdgcn_s_setprio(1); else __builtin_amdgcn_s_setprio(0);
;             const unsigned char* eb = F.ED + s * SLICE_B;
;             const unsigned lo = (unsigned)(c8 * 16);
;             v4u wA[8], wB[8];
;     ...
;             P9A_LOAD(wA, 0, 0);
; #pragma unroll
;             for (int j = 0; j < 8; ++j) {
;                 P9A_LOAD(wB, j, 1);
;                 P9A_COMP(wA, j, 0);
;                 if (j < 7) P9A_LOAD(wA, j + 1, 0);
;                 P9A_COMP(wB, j, 1);
;             }
.LBB0_1302:
	ds_read_b128 v[26:29], v181 offset:128
	s_add_u32 s46, s37, s44
	s_addc_u32 s47, s39, s45
	v_mov_b32_e32 v91, 0
	s_waitcnt lgkmcnt(1)
	ds_read_b128 v[58:61], v2
	v_mov_b32_e32 v3, 0
	v_mov_b32_e32 v93, 0
	v_mov_b32_e32 v5, 0
	v_mov_b32_e32 v4, 0
	v_mov_b32_e32 v90, 0
	v_mov_b32_e32 v92, 0
	v_mov_b32_e32 v94, 0
	s_waitcnt lgkmcnt(1)
	v_lshlrev_b32_sdwa v62, v198, v26 dst_sel:DWORD dst_unused:UNUSED_PAD src0_sel:DWORD src1_sel:WORD_1
	v_lshlrev_b32_sdwa v26, v198, v26 dst_sel:DWORD dst_unused:UNUSED_PAD src0_sel:DWORD src1_sel:WORD_0
	v_lshlrev_b32_sdwa v63, v198, v27 dst_sel:DWORD dst_unused:UNUSED_PAD src0_sel:DWORD src1_sel:WORD_1
	v_lshlrev_b32_sdwa v27, v198, v27 dst_sel:DWORD dst_unused:UNUSED_PAD src0_sel:DWORD src1_sel:WORD_0
	v_lshlrev_b32_sdwa v64, v198, v28 dst_sel:DWORD dst_unused:UNUSED_PAD src0_sel:DWORD src1_sel:WORD_1
	v_lshlrev_b32_sdwa v28, v198, v28 dst_sel:DWORD dst_unused:UNUSED_PAD src0_sel:DWORD src1_sel:WORD_0
	v_lshlrev_b32_sdwa v65, v198, v29 dst_sel:DWORD dst_unused:UNUSED_PAD src0_sel:DWORD src1_sel:WORD_1
	v_lshlrev_b32_sdwa v29, v198, v29 dst_sel:DWORD dst_unused:UNUSED_PAD src0_sel:DWORD src1_sel:WORD_0
	v_or_b32_e32 v62, v62, v1
	v_or_b32_e32 v26, v26, v130
	v_or_b32_e32 v70, v63, v1
	v_or_b32_e32 v66, v27, v130
	v_or_b32_e32 v78, v64, v1
	v_or_b32_e32 v74, v28, v130
	v_or_b32_e32 v86, v65, v1
	v_or_b32_e32 v82, v29, v130
	global_load_dwordx4 v[26:29], v26, s[46:47]
	s_nop 0
	global_load_dwordx4 v[62:65], v62, s[46:47]
	s_nop 0
	global_load_dwordx4 v[66:69], v66, s[46:47]
	s_nop 0
	global_load_dwordx4 v[70:73], v70, s[46:47]
	s_nop 0
	global_load_dwordx4 v[74:77], v74, s[46:47]
	s_nop 0
	global_load_dwordx4 v[78:81], v78, s[46:47]
	s_nop 0
	global_load_dwordx4 v[82:85], v82, s[46:47]
	s_nop 0
	global_load_dwordx4 v[86:89], v86, s[46:47]
	s_add_i32 s23, s23, 1
	s_add_u32 s44, s44, 0x80
	s_addc_u32 s45, s45, 0
	s_cmpk_eq_i32 s44, 0x800
	s_waitcnt vmcnt(8)
	v_mov_b64_e32 v[30:31], v[220:221]
	v_mov_b64_e32 v[32:33], v[222:223]
	v_mov_b64_e32 v[34:35], v[224:225]
	v_mov_b64_e32 v[36:37], v[226:227]
	v_mov_b64_e32 v[38:39], v[228:229]
	v_mov_b64_e32 v[40:41], v[230:231]
	v_mov_b64_e32 v[42:43], v[232:233]
	v_mov_b64_e32 v[44:45], v[234:235]
	v_mov_b64_e32 v[46:47], v[236:237]
	v_mov_b64_e32 v[48:49], v[238:239]
	v_mov_b64_e32 v[50:51], v[240:241]
	v_mov_b64_e32 v[52:53], v[242:243]
	v_mov_b64_e32 v[22:23], v[244:245]
	v_mov_b64_e32 v[24:25], v[246:247]
	v_mov_b64_e32 v[54:55], v[248:249]
	v_mov_b64_e32 v[56:57], v[250:251]
	s_waitcnt vmcnt(15) lgkmcnt(0)
	v_dot4c_i32_i8_e32 v3, v58, v30
	v_dot4c_i32_i8_e32 v3, v59, v31
	v_dot4c_i32_i8_e32 v3, v60, v32
	v_dot4c_i32_i8_e32 v3, v61, v33
	s_waitcnt vmcnt(14)
	v_dot4c_i32_i8_e32 v4, v58, v34
	s_waitcnt vmcnt(13)
	v_dot4c_i32_i8_e32 v5, v58, v38
	s_waitcnt vmcnt(12)
	v_dot4c_i32_i8_e32 v90, v58, v42
	v_dot4c_i32_i8_e32 v5, v59, v39
	v_dot4c_i32_i8_e32 v4, v59, v35
	v_dot4c_i32_i8_e32 v90, v59, v43
	s_waitcnt vmcnt(11)
	v_dot4c_i32_i8_e32 v91, v58, v46
	v_dot4c_i32_i8_e32 v91, v59, v47
	v_dot4c_i32_i8_e32 v91, v60, v48
	v_dot4c_i32_i8_e32 v91, v61, v49
	s_waitcnt vmcnt(10)
	v_dot4c_i32_i8_e32 v92, v58, v50
	s_waitcnt vmcnt(9)
	v_dot4c_i32_i8_e32 v93, v58, v22
	s_waitcnt vmcnt(8)
	v_dot4c_i32_i8_e32 v94, v58, v54
	v_cndmask_b32_e64 v22, v3, v91, s[2:3]
	ds_bpermute_b32 v22, v159, v22
	v_dot4c_i32_i8_e32 v93, v59, v23
	v_dot4c_i32_i8_e32 v92, v59, v51
	v_dot4c_i32_i8_e32 v94, v59, v55
	v_dot4c_i32_i8_e32 v5, v60, v40
	v_dot4c_i32_i8_e32 v93, v60, v24
	v_dot4c_i32_i8_e32 v4, v60, v36
	v_dot4c_i32_i8_e32 v90, v60, v44
	v_dot4c_i32_i8_e32 v92, v60, v52
	v_dot4c_i32_i8_e32 v94, v60, v56
	v_dot4c_i32_i8_e32 v5, v61, v41
	v_dot4c_i32_i8_e32 v93, v61, v25
	v_cndmask_b32_e64 v3, v91, v3, s[2:3]
	v_dot4c_i32_i8_e32 v4, v61, v37
	v_dot4c_i32_i8_e32 v90, v61, v45
	v_dot4c_i32_i8_e32 v92, v61, v53
	v_dot4c_i32_i8_e32 v94, v61, v57
	s_waitcnt lgkmcnt(0)
	v_add_u32_e32 v3, v3, v22
	v_cndmask_b32_e64 v22, v5, v93, s[2:3]
	v_cndmask_b32_e64 v23, v92, v4, s[2:3]
	v_cndmask_b32_e64 v4, v4, v92, s[2:3]
	ds_bpermute_b32 v22, v159, v22
	v_cndmask_b32_e64 v24, v90, v94, s[2:3]
	ds_bpermute_b32 v4, v159, v4
	ds_bpermute_b32 v24, v159, v24
	v_cndmask_b32_e64 v5, v93, v5, s[2:3]
	s_waitcnt lgkmcnt(2)
	v_add_u32_e32 v5, v5, v22
	v_cndmask_b32_e64 v22, v94, v90, s[2:3]
	s_waitcnt lgkmcnt(1)
	v_add_u32_e32 v4, v23, v4
	s_waitcnt lgkmcnt(0)
	v_add_u32_e32 v22, v22, v24
	v_cndmask_b32_e64 v23, v3, v5, s[4:5]
	v_cndmask_b32_e64 v24, v4, v22, s[4:5]
	ds_bpermute_b32 v23, v160, v23
	ds_bpermute_b32 v24, v160, v24
	v_cndmask_b32_e64 v3, v5, v3, s[4:5]
	v_cndmask_b32_e64 v4, v22, v4, s[4:5]
	v_mov_b32_e32 v90, 0
	s_waitcnt lgkmcnt(1)
	v_add_u32_e32 v3, v3, v23
	s_waitcnt lgkmcnt(0)
	v_add_u32_e32 v4, v4, v24
	v_cndmask_b32_e64 v5, v3, v4, s[6:7]
	ds_bpermute_b32 v5, v161, v5
	ds_read_b128 v[22:25], v181 offset:256
	v_cndmask_b32_e64 v3, v4, v3, s[6:7]
	s_waitcnt lgkmcnt(1)
	v_add3_u32 v6, v5, v6, v3
	s_waitcnt lgkmcnt(0)
; #define P9A_LOAD(W, J, H) do { _Pragma("unroll") for (int i = 0; i < 8; ++i) { const unsigned e = IDX16[(F.wave * 8 + (J)) * 128 + 64 * (H) + 8 * g + i]; W[i] = *(const GAS v4u*)(eb + (e * 2048u + lo)); } } while (0)
; DI void p9v2_phase(Frame& F) {
;     ...
;             P9A_LOAD(wA, 0, 0);
; #pragma unroll
;             for (int j = 0; j < 8; ++j) {
;                 P9A_LOAD(wB, j, 1);
;                 P9A_COMP(wA, j, 0);
;                 if (j < 7) P9A_LOAD(wA, j + 1, 0);
;                 P9A_COMP(wB, j, 1);
;             }
	v_lshlrev_b32_sdwa v3, v198, v25 dst_sel:DWORD dst_unused:UNUSED_PAD src0_sel:DWORD src1_sel:WORD_1
	v_lshlrev_b32_sdwa v4, v198, v25 dst_sel:DWORD dst_unused:UNUSED_PAD src0_sel:DWORD src1_sel:WORD_0
	v_or_b32_e32 v3, v3, v1
	v_or_b32_e32 v4, v4, v130
	global_load_dwordx4 v[30:33], v3, s[46:47]
	global_load_dwordx4 v[34:37], v4, s[46:47]
	v_lshlrev_b32_sdwa v3, v198, v24 dst_sel:DWORD dst_unused:UNUSED_PAD src0_sel:DWORD src1_sel:WORD_1
	v_lshlrev_b32_sdwa v4, v198, v24 dst_sel:DWORD dst_unused:UNUSED_PAD src0_sel:DWORD src1_sel:WORD_0
	v_or_b32_e32 v3, v3, v1
	v_or_b32_e32 v4, v4, v130
	global_load_dwordx4 v[38:41], v3, s[46:47]
	global_load_dwordx4 v[42:45], v4, s[46:47]
	v_lshlrev_b32_sdwa v3, v198, v23 dst_sel:DWORD dst_unused:UNUSED_PAD src0_sel:DWORD src1_sel:WORD_1
	v_lshlrev_b32_sdwa v4, v198, v23 dst_sel:DWORD dst_unused:UNUSED_PAD src0_sel:DWORD src1_sel:WORD_0
	v_or_b32_e32 v3, v3, v1
	v_or_b32_e32 v4, v4, v130
	global_load_dwordx4 v[46:49], v3, s[46:47]
	global_load_dwordx4 v[50:53], v4, s[46:47]
	v_lshlrev_b32_sdwa v3, v198, v22 dst_sel:DWORD dst_unused:UNUSED_PAD src0_sel:DWORD src1_sel:WORD_1
	v_lshlrev_b32_sdwa v4, v198, v22 dst_sel:DWORD dst_unused:UNUSED_PAD src0_sel:DWORD src1_sel:WORD_0
	v_or_b32_e32 v3, v3, v1
	ds_read_b128 v[22:25], v2
	v_or_b32_e32 v4, v4, v130
	global_load_dwordx4 v[54:57], v3, s[46:47]
	global_load_dwordx4 v[58:61], v4, s[46:47]
	v_mov_b32_e32 v3, 0
	v_mov_b32_e32 v4, 0
	s_waitcnt vmcnt(15) lgkmcnt(0)
	v_dot4c_i32_i8_e32 v3, v22, v26
	v_dot4c_i32_i8_e32 v3, v23, v27
	v_mov_b32_e32 v27, 0
	s_waitcnt vmcnt(11)
	v_dot4c_i32_i8_e32 v27, v22, v74
	v_dot4c_i32_i8_e32 v27, v23, v75
	v_dot4c_i32_i8_e32 v3, v24, v28
	v_dot4c_i32_i8_e32 v27, v24, v76
	v_dot4c_i32_i8_e32 v3, v25, v29
	v_dot4c_i32_i8_e32 v4, v22, v62
	v_mov_b32_e32 v5, 0
	v_mov_b32_e32 v26, 0
	v_dot4c_i32_i8_e32 v27, v25, v77
	v_mov_b32_e32 v28, 0
	v_mov_b32_e32 v29, 0
	v_mov_b32_e32 v62, 0
	v_dot4c_i32_i8_e32 v5, v22, v66
	v_dot4c_i32_i8_e32 v26, v22, v70
	s_waitcnt vmcnt(10)
	v_dot4c_i32_i8_e32 v28, v22, v78
	s_waitcnt vmcnt(9)
	v_dot4c_i32_i8_e32 v29, v22, v82
	s_waitcnt vmcnt(8)
	v_dot4c_i32_i8_e32 v62, v22, v86
	v_cndmask_b32_e64 v22, v3, v27, s[2:3]
	ds_bpermute_b32 v22, v159, v22
	v_dot4c_i32_i8_e32 v4, v23, v63
	v_dot4c_i32_i8_e32 v28, v23, v79
	v_dot4c_i32_i8_e32 v4, v24, v64
	v_dot4c_i32_i8_e32 v5, v23, v67
	v_dot4c_i32_i8_e32 v26, v23, v71
	v_dot4c_i32_i8_e32 v28, v24, v80
	v_dot4c_i32_i8_e32 v29, v23, v83
	v_dot4c_i32_i8_e32 v62, v23, v87
	v_dot4c_i32_i8_e32 v4, v25, v65
	v_dot4c_i32_i8_e32 v5, v24, v68
	v_dot4c_i32_i8_e32 v26, v24, v72
	v_dot4c_i32_i8_e32 v28, v25, v81
	v_dot4c_i32_i8_e32 v29, v24, v84
	v_dot4c_i32_i8_e32 v62, v24, v88
	v_cndmask_b32_e64 v3, v27, v3, s[2:3]
	v_dot4c_i32_i8_e32 v5, v25, v69
	v_dot4c_i32_i8_e32 v26, v25, v73
	v_dot4c_i32_i8_e32 v29, v25, v85
	v_dot4c_i32_i8_e32 v62, v25, v89
	s_waitcnt lgkmcnt(0)
	v_add_u32_e32 v3, v3, v22
	v_cndmask_b32_e64 v22, v28, v4, s[2:3]
	v_cndmask_b32_e64 v4, v4, v28, s[2:3]
	ds_bpermute_b32 v4, v159, v4
	v_cndmask_b32_e64 v23, v5, v29, s[2:3]
	v_cndmask_b32_e64 v24, v26, v62, s[2:3]
	ds_bpermute_b32 v23, v159, v23
	ds_bpermute_b32 v24, v159, v24
	s_waitcnt lgkmcnt(2)
	v_add_u32_e32 v4, v22, v4
	v_cndmask_b32_e64 v5, v29, v5, s[2:3]
	v_cndmask_b32_e64 v22, v62, v26, s[2:3]
	s_waitcnt lgkmcnt(1)
	v_add_u32_e32 v5, v5, v23
	s_waitcnt lgkmcnt(0)
	v_add_u32_e32 v26, v22, v24
	ds_read_b128 v[22:25], v181 offset:384
	v_cndmask_b32_e64 v27, v5, v3, s[4:5]
	v_cndmask_b32_e64 v3, v3, v5, s[4:5]
	ds_bpermute_b32 v3, v160, v3
	v_cndmask_b32_e64 v5, v4, v26, s[4:5]
	v_cndmask_b32_e64 v4, v26, v4, s[4:5]
	s_waitcnt lgkmcnt(1)
	v_lshlrev_b32_sdwa v26, v198, v22 dst_sel:DWORD dst_unused:UNUSED_PAD src0_sel:DWORD src1_sel:WORD_1
	v_lshlrev_b32_sdwa v22, v198, v22 dst_sel:DWORD dst_unused:UNUSED_PAD src0_sel:DWORD src1_sel:WORD_0
	v_or_b32_e32 v62, v26, v1
	v_or_b32_e32 v22, v22, v130
	s_waitcnt lgkmcnt(0)
	v_add_u32_e32 v3, v27, v3
	global_load_dwordx4 v[26:29], v22, s[46:47]
	s_nop 0
	global_load_dwordx4 v[62:65], v62, s[46:47]
	v_lshlrev_b32_sdwa v22, v198, v23 dst_sel:DWORD dst_unused:UNUSED_PAD src0_sel:DWORD src1_sel:WORD_1
	v_lshlrev_b32_sdwa v23, v198, v23 dst_sel:DWORD dst_unused:UNUSED_PAD src0_sel:DWORD src1_sel:WORD_0
	v_or_b32_e32 v22, v22, v1
	v_or_b32_e32 v23, v23, v130
	global_load_dwordx4 v[66:69], v23, s[46:47]
	global_load_dwordx4 v[70:73], v22, s[46:47]
	v_lshlrev_b32_sdwa v22, v198, v24 dst_sel:DWORD dst_unused:UNUSED_PAD src0_sel:DWORD src1_sel:WORD_1
	v_lshlrev_b32_sdwa v23, v198, v24 dst_sel:DWORD dst_unused:UNUSED_PAD src0_sel:DWORD src1_sel:WORD_0
	v_or_b32_e32 v22, v22, v1
	v_or_b32_e32 v23, v23, v130
	global_load_dwordx4 v[74:77], v23, s[46:47]
	global_load_dwordx4 v[78:81], v22, s[46:47]
	v_lshlrev_b32_sdwa v22, v198, v25 dst_sel:DWORD dst_unused:UNUSED_PAD src0_sel:DWORD src1_sel:WORD_1
	v_lshlrev_b32_sdwa v82, v198, v25 dst_sel:DWORD dst_unused:UNUSED_PAD src0_sel:DWORD src1_sel:WORD_0
	v_or_b32_e32 v86, v22, v1
	ds_read_b128 v[22:25], v2 offset:2048
	v_or_b32_e32 v82, v82, v130
	global_load_dwordx4 v[82:85], v82, s[46:47]
	s_nop 0
	global_load_dwordx4 v[86:89], v86, s[46:47]
	ds_bpermute_b32 v5, v160, v5
	s_waitcnt vmcnt(8) lgkmcnt(1)
; #define P9A_LOAD(W, J, H) do { _Pragma("unroll") for (int i = 0; i < 8; ++i) { const unsigned e = IDX16[(F.wave * 8 + (J)) * 128 + 64 * (H) + 8 * g + i]; W[i] = *(const GAS v4u*)(eb + (e * 2048u + lo)); } } while (0)
; DI void p9v2_phase(Frame& F) {
;     ...
;             P9A_LOAD(wA, 0, 0);
; #pragma unroll
;             for (int j = 0; j < 8; ++j) {
;                 P9A_LOAD(wB, j, 1);
;                 P9A_COMP(wA, j, 0);
;                 if (j < 7) P9A_LOAD(wA, j + 1, 0);
;                 P9A_COMP(wB, j, 1);
;             }
	v_dot4c_i32_i8_e32 v90, v22, v58
	v_mov_b32_e32 v58, 0
	v_dot4c_i32_i8_e32 v58, v22, v54
	v_mov_b32_e32 v54, 0
	v_dot4c_i32_i8_e32 v54, v22, v50
	v_mov_b32_e32 v50, 0
	v_dot4c_i32_i8_e32 v50, v22, v46
	v_mov_b32_e32 v46, 0
	v_dot4c_i32_i8_e32 v46, v22, v42
	v_mov_b32_e32 v42, 0
	v_dot4c_i32_i8_e32 v90, v23, v59
	v_dot4c_i32_i8_e32 v46, v23, v43
	v_dot4c_i32_i8_e32 v42, v22, v38
	v_mov_b32_e32 v38, 0
	v_dot4c_i32_i8_e32 v90, v24, v60
	v_dot4c_i32_i8_e32 v58, v23, v55
	v_dot4c_i32_i8_e32 v46, v24, v44
	v_dot4c_i32_i8_e32 v42, v23, v39
	v_dot4c_i32_i8_e32 v38, v22, v34
	v_mov_b32_e32 v34, 0
	v_dot4c_i32_i8_e32 v90, v25, v61
	v_dot4c_i32_i8_e32 v58, v24, v56
	v_dot4c_i32_i8_e32 v54, v23, v51
	v_dot4c_i32_i8_e32 v46, v25, v45
	v_dot4c_i32_i8_e32 v42, v24, v40
	v_dot4c_i32_i8_e32 v38, v23, v35
	v_dot4c_i32_i8_e32 v34, v22, v30
	v_dot4c_i32_i8_e32 v58, v25, v57
	v_dot4c_i32_i8_e32 v54, v24, v52
	v_dot4c_i32_i8_e32 v50, v23, v47
	v_dot4c_i32_i8_e32 v42, v25, v41
	v_dot4c_i32_i8_e32 v38, v24, v36
	v_cndmask_b32_e64 v22, v90, v46, s[2:3]
	v_dot4c_i32_i8_e32 v34, v23, v31
	v_dot4c_i32_i8_e32 v54, v25, v53
	v_dot4c_i32_i8_e32 v50, v24, v48
	v_dot4c_i32_i8_e32 v38, v25, v37
	ds_bpermute_b32 v22, v159, v22
	v_dot4c_i32_i8_e32 v34, v24, v32
	v_cndmask_b32_e64 v24, v58, v42, s[2:3]
	v_dot4c_i32_i8_e32 v50, v25, v49
	v_dot4c_i32_i8_e32 v34, v25, v33
	ds_bpermute_b32 v24, v159, v24
	v_cndmask_b32_e64 v25, v54, v38, s[2:3]
	ds_bpermute_b32 v25, v159, v25
	v_cndmask_b32_e64 v30, v50, v34, s[2:3]
	ds_bpermute_b32 v30, v159, v30
	v_cndmask_b32_e64 v23, v46, v90, s[2:3]
	s_waitcnt lgkmcnt(3)
	v_add_u32_e32 v22, v23, v22
	v_cndmask_b32_e64 v23, v42, v58, s[2:3]
	s_waitcnt lgkmcnt(2)
	v_add_u32_e32 v23, v23, v24
	v_cndmask_b32_e64 v24, v38, v54, s[2:3]
	s_waitcnt lgkmcnt(1)
	v_add_u32_e32 v24, v24, v25
	v_cndmask_b32_e64 v25, v34, v50, s[2:3]
	s_waitcnt lgkmcnt(0)
	v_add_u32_e32 v25, v25, v30
	v_cndmask_b32_e64 v30, v22, v24, s[4:5]
	ds_bpermute_b32 v30, v160, v30
	v_cndmask_b32_e64 v31, v23, v25, s[4:5]
	ds_bpermute_b32 v31, v160, v31
	v_cndmask_b32_e64 v22, v24, v22, s[4:5]
	v_add_u32_e32 v4, v4, v5
	s_waitcnt lgkmcnt(1)
	v_add_u32_e32 v30, v22, v30
	v_cndmask_b32_e64 v22, v25, v23, s[4:5]
	v_cndmask_b32_e64 v5, v3, v4, s[6:7]
	s_waitcnt lgkmcnt(0)
	v_add_u32_e32 v31, v22, v31
	ds_bpermute_b32 v5, v161, v5
	v_cndmask_b32_e64 v22, v30, v31, s[6:7]
	ds_bpermute_b32 v32, v161, v22
	ds_read_b128 v[22:25], v181 offset:512
	v_cndmask_b32_e64 v3, v4, v3, s[6:7]
	s_waitcnt lgkmcnt(2)
	v_add3_u32 v7, v5, v7, v3
	v_cndmask_b32_e64 v3, v31, v30, s[6:7]
	s_waitcnt lgkmcnt(1)
	v_add3_u32 v8, v32, v8, v3
	s_waitcnt lgkmcnt(0)
	v_lshlrev_b32_sdwa v3, v198, v25 dst_sel:DWORD dst_unused:UNUSED_PAD src0_sel:DWORD src1_sel:WORD_1
	v_lshlrev_b32_sdwa v4, v198, v25 dst_sel:DWORD dst_unused:UNUSED_PAD src0_sel:DWORD src1_sel:WORD_0
	v_or_b32_e32 v3, v3, v1
	v_or_b32_e32 v4, v4, v130
	global_load_dwordx4 v[30:33], v3, s[46:47]
	global_load_dwordx4 v[34:37], v4, s[46:47]
	v_lshlrev_b32_sdwa v3, v198, v24 dst_sel:DWORD dst_unused:UNUSED_PAD src0_sel:DWORD src1_sel:WORD_1
	v_lshlrev_b32_sdwa v4, v198, v24 dst_sel:DWORD dst_unused:UNUSED_PAD src0_sel:DWORD src1_sel:WORD_0
	v_or_b32_e32 v3, v3, v1
	v_or_b32_e32 v4, v4, v130
	global_load_dwordx4 v[38:41], v3, s[46:47]
	global_load_dwordx4 v[42:45], v4, s[46:47]
	v_lshlrev_b32_sdwa v3, v198, v23 dst_sel:DWORD dst_unused:UNUSED_PAD src0_sel:DWORD src1_sel:WORD_1
	v_lshlrev_b32_sdwa v4, v198, v23 dst_sel:DWORD dst_unused:UNUSED_PAD src0_sel:DWORD src1_sel:WORD_0
	v_or_b32_e32 v3, v3, v1
	v_or_b32_e32 v4, v4, v130
	global_load_dwordx4 v[46:49], v3, s[46:47]
	global_load_dwordx4 v[50:53], v4, s[46:47]
	v_lshlrev_b32_sdwa v3, v198, v22 dst_sel:DWORD dst_unused:UNUSED_PAD src0_sel:DWORD src1_sel:WORD_1
	v_lshlrev_b32_sdwa v4, v198, v22 dst_sel:DWORD dst_unused:UNUSED_PAD src0_sel:DWORD src1_sel:WORD_0
	v_or_b32_e32 v3, v3, v1
	ds_read_b128 v[22:25], v2 offset:2048
	v_or_b32_e32 v4, v4, v130
	global_load_dwordx4 v[54:57], v3, s[46:47]
	global_load_dwordx4 v[58:61], v4, s[46:47]
	v_mov_b32_e32 v3, 0
	v_mov_b32_e32 v4, 0
	s_waitcnt vmcnt(15) lgkmcnt(0)
	v_dot4c_i32_i8_e32 v3, v22, v26
	v_dot4c_i32_i8_e32 v3, v23, v27
	v_mov_b32_e32 v27, 0
	s_waitcnt vmcnt(11)
	v_dot4c_i32_i8_e32 v27, v22, v74
	v_dot4c_i32_i8_e32 v27, v23, v75
	v_dot4c_i32_i8_e32 v3, v24, v28
	v_dot4c_i32_i8_e32 v27, v24, v76
	v_dot4c_i32_i8_e32 v3, v25, v29
	v_dot4c_i32_i8_e32 v4, v22, v62
	v_mov_b32_e32 v5, 0
	v_mov_b32_e32 v26, 0
	v_dot4c_i32_i8_e32 v27, v25, v77
	v_mov_b32_e32 v28, 0
	v_mov_b32_e32 v29, 0
	v_mov_b32_e32 v62, 0
	v_dot4c_i32_i8_e32 v5, v22, v66
	v_dot4c_i32_i8_e32 v26, v22, v70
	s_waitcnt vmcnt(10)
	v_dot4c_i32_i8_e32 v28, v22, v78
	s_waitcnt vmcnt(9)
	v_dot4c_i32_i8_e32 v29, v22, v82
	s_waitcnt vmcnt(8)
	v_dot4c_i32_i8_e32 v62, v22, v86
	v_cndmask_b32_e64 v22, v3, v27, s[2:3]
	ds_bpermute_b32 v22, v159, v22
	v_dot4c_i32_i8_e32 v4, v23, v63
	v_dot4c_i32_i8_e32 v28, v23, v79
	v_dot4c_i32_i8_e32 v4, v24, v64
	v_dot4c_i32_i8_e32 v5, v23, v67
	v_dot4c_i32_i8_e32 v26, v23, v71
	v_dot4c_i32_i8_e32 v28, v24, v80
	v_dot4c_i32_i8_e32 v29, v23, v83
	v_dot4c_i32_i8_e32 v62, v23, v87
	v_dot4c_i32_i8_e32 v4, v25, v65
	v_dot4c_i32_i8_e32 v5, v24, v68
	v_dot4c_i32_i8_e32 v26, v24, v72
	v_dot4c_i32_i8_e32 v28, v25, v81
	v_dot4c_i32_i8_e32 v29, v24, v84
	v_dot4c_i32_i8_e32 v62, v24, v88
	v_cndmask_b32_e64 v3, v27, v3, s[2:3]
	v_dot4c_i32_i8_e32 v5, v25, v69
	v_dot4c_i32_i8_e32 v26, v25, v73
	v_dot4c_i32_i8_e32 v29, v25, v85
	v_dot4c_i32_i8_e32 v62, v25, v89
	s_waitcnt lgkmcnt(0)
; #define P9A_LOAD(W, J, H) do { _Pragma("unroll") for (int i = 0; i < 8; ++i) { const unsigned e = IDX16[(F.wave * 8 + (J)) * 128 + 64 * (H) + 8 * g + i]; W[i] = *(const GAS v4u*)(eb + (e * 2048u + lo)); } } while (0)
; DI void p9v2_phase(Frame& F) {
;     ...
;             P9A_LOAD(wA, 0, 0);
; #pragma unroll
;             for (int j = 0; j < 8; ++j) {
;                 P9A_LOAD(wB, j, 1);
;                 P9A_COMP(wA, j, 0);
;                 if (j < 7) P9A_LOAD(wA, j + 1, 0);
;                 P9A_COMP(wB, j, 1);
;             }
	v_add_u32_e32 v3, v3, v22
	v_cndmask_b32_e64 v22, v28, v4, s[2:3]
	v_cndmask_b32_e64 v4, v4, v28, s[2:3]
	ds_bpermute_b32 v4, v159, v4
	v_cndmask_b32_e64 v23, v5, v29, s[2:3]
	v_cndmask_b32_e64 v24, v26, v62, s[2:3]
	ds_bpermute_b32 v23, v159, v23
	ds_bpermute_b32 v24, v159, v24
	s_waitcnt lgkmcnt(2)
	v_add_u32_e32 v4, v22, v4
	v_cndmask_b32_e64 v5, v29, v5, s[2:3]
	v_cndmask_b32_e64 v22, v62, v26, s[2:3]
	s_waitcnt lgkmcnt(1)
	v_add_u32_e32 v5, v5, v23
	s_waitcnt lgkmcnt(0)
	v_add_u32_e32 v26, v22, v24
	ds_read_b128 v[22:25], v181 offset:640
	v_cndmask_b32_e64 v27, v5, v3, s[4:5]
	v_cndmask_b32_e64 v3, v3, v5, s[4:5]
	ds_bpermute_b32 v3, v160, v3
	v_cndmask_b32_e64 v5, v4, v26, s[4:5]
	v_cndmask_b32_e64 v4, v26, v4, s[4:5]
	s_waitcnt lgkmcnt(1)
	v_lshlrev_b32_sdwa v26, v198, v22 dst_sel:DWORD dst_unused:UNUSED_PAD src0_sel:DWORD src1_sel:WORD_1
	v_lshlrev_b32_sdwa v22, v198, v22 dst_sel:DWORD dst_unused:UNUSED_PAD src0_sel:DWORD src1_sel:WORD_0
	v_or_b32_e32 v62, v26, v1
	v_or_b32_e32 v22, v22, v130
	s_waitcnt lgkmcnt(0)
	v_add_u32_e32 v3, v27, v3
	global_load_dwordx4 v[26:29], v22, s[46:47]
	s_nop 0
	global_load_dwordx4 v[62:65], v62, s[46:47]
	v_lshlrev_b32_sdwa v22, v198, v23 dst_sel:DWORD dst_unused:UNUSED_PAD src0_sel:DWORD src1_sel:WORD_1
	v_lshlrev_b32_sdwa v23, v198, v23 dst_sel:DWORD dst_unused:UNUSED_PAD src0_sel:DWORD src1_sel:WORD_0
	v_or_b32_e32 v22, v22, v1
	v_or_b32_e32 v23, v23, v130
	global_load_dwordx4 v[66:69], v23, s[46:47]
	global_load_dwordx4 v[70:73], v22, s[46:47]
	v_lshlrev_b32_sdwa v22, v198, v24 dst_sel:DWORD dst_unused:UNUSED_PAD src0_sel:DWORD src1_sel:WORD_1
	v_lshlrev_b32_sdwa v23, v198, v24 dst_sel:DWORD dst_unused:UNUSED_PAD src0_sel:DWORD src1_sel:WORD_0
	v_or_b32_e32 v22, v22, v1
	v_or_b32_e32 v23, v23, v130
	global_load_dwordx4 v[74:77], v23, s[46:47]
	global_load_dwordx4 v[78:81], v22, s[46:47]
	v_lshlrev_b32_sdwa v22, v198, v25 dst_sel:DWORD dst_unused:UNUSED_PAD src0_sel:DWORD src1_sel:WORD_1
	v_lshlrev_b32_sdwa v82, v198, v25 dst_sel:DWORD dst_unused:UNUSED_PAD src0_sel:DWORD src1_sel:WORD_0
	v_or_b32_e32 v86, v22, v1
	ds_read_b128 v[22:25], v2 offset:4096
	v_mov_b32_e32 v90, 0
	v_or_b32_e32 v82, v82, v130
	global_load_dwordx4 v[82:85], v82, s[46:47]
	s_nop 0
	global_load_dwordx4 v[86:89], v86, s[46:47]
	ds_bpermute_b32 v5, v160, v5
	s_waitcnt vmcnt(8) lgkmcnt(1)
	v_dot4c_i32_i8_e32 v90, v22, v58
	v_mov_b32_e32 v58, 0
	v_dot4c_i32_i8_e32 v58, v22, v54
	v_mov_b32_e32 v54, 0
	v_dot4c_i32_i8_e32 v54, v22, v50
	v_mov_b32_e32 v50, 0
	v_dot4c_i32_i8_e32 v50, v22, v46
	v_mov_b32_e32 v46, 0
	v_dot4c_i32_i8_e32 v46, v22, v42
	v_mov_b32_e32 v42, 0
	v_dot4c_i32_i8_e32 v90, v23, v59
	v_dot4c_i32_i8_e32 v46, v23, v43
	v_dot4c_i32_i8_e32 v42, v22, v38
	v_mov_b32_e32 v38, 0
	v_dot4c_i32_i8_e32 v90, v24, v60
	v_dot4c_i32_i8_e32 v58, v23, v55
	v_dot4c_i32_i8_e32 v46, v24, v44
	v_dot4c_i32_i8_e32 v42, v23, v39
	v_dot4c_i32_i8_e32 v38, v22, v34
	v_mov_b32_e32 v34, 0
	v_dot4c_i32_i8_e32 v90, v25, v61
	v_dot4c_i32_i8_e32 v58, v24, v56
	v_dot4c_i32_i8_e32 v54, v23, v51
	v_dot4c_i32_i8_e32 v46, v25, v45
	v_dot4c_i32_i8_e32 v42, v24, v40
	v_dot4c_i32_i8_e32 v38, v23, v35
	v_dot4c_i32_i8_e32 v34, v22, v30
	v_dot4c_i32_i8_e32 v58, v25, v57
	v_dot4c_i32_i8_e32 v54, v24, v52
	v_dot4c_i32_i8_e32 v50, v23, v47
	v_dot4c_i32_i8_e32 v42, v25, v41
	v_dot4c_i32_i8_e32 v38, v24, v36
	v_cndmask_b32_e64 v22, v90, v46, s[2:3]
	v_dot4c_i32_i8_e32 v34, v23, v31
	v_dot4c_i32_i8_e32 v54, v25, v53
	v_dot4c_i32_i8_e32 v50, v24, v48
	v_dot4c_i32_i8_e32 v38, v25, v37
	ds_bpermute_b32 v22, v159, v22
	v_dot4c_i32_i8_e32 v34, v24, v32
	v_cndmask_b32_e64 v24, v58, v42, s[2:3]
	v_dot4c_i32_i8_e32 v50, v25, v49
	v_dot4c_i32_i8_e32 v34, v25, v33
	ds_bpermute_b32 v24, v159, v24
	v_cndmask_b32_e64 v25, v54, v38, s[2:3]
	ds_bpermute_b32 v25, v159, v25
	v_cndmask_b32_e64 v30, v50, v34, s[2:3]
	ds_bpermute_b32 v30, v159, v30
	v_cndmask_b32_e64 v23, v46, v90, s[2:3]
	s_waitcnt lgkmcnt(3)
	v_add_u32_e32 v22, v23, v22
	v_cndmask_b32_e64 v23, v42, v58, s[2:3]
	s_waitcnt lgkmcnt(2)
	v_add_u32_e32 v23, v23, v24
	v_cndmask_b32_e64 v24, v38, v54, s[2:3]
	s_waitcnt lgkmcnt(1)
	v_add_u32_e32 v24, v24, v25
	v_cndmask_b32_e64 v25, v34, v50, s[2:3]
	s_waitcnt lgkmcnt(0)
	v_add_u32_e32 v25, v25, v30
	v_cndmask_b32_e64 v30, v22, v24, s[4:5]
	ds_bpermute_b32 v30, v160, v30
	v_cndmask_b32_e64 v31, v23, v25, s[4:5]
	ds_bpermute_b32 v31, v160, v31
	v_cndmask_b32_e64 v22, v24, v22, s[4:5]
	v_add_u32_e32 v4, v4, v5
	s_waitcnt lgkmcnt(1)
	v_add_u32_e32 v30, v22, v30
	v_cndmask_b32_e64 v22, v25, v23, s[4:5]
	v_cndmask_b32_e64 v5, v3, v4, s[6:7]
	s_waitcnt lgkmcnt(0)
	v_add_u32_e32 v31, v22, v31
	ds_bpermute_b32 v5, v161, v5
	v_cndmask_b32_e64 v22, v30, v31, s[6:7]
	ds_bpermute_b32 v32, v161, v22
	ds_read_b128 v[22:25], v181 offset:768
	v_cndmask_b32_e64 v3, v4, v3, s[6:7]
	s_waitcnt lgkmcnt(2)
	v_add3_u32 v9, v5, v9, v3
	v_cndmask_b32_e64 v3, v31, v30, s[6:7]
	s_waitcnt lgkmcnt(1)
	v_add3_u32 v10, v32, v10, v3
	s_waitcnt lgkmcnt(0)
; #define P9A_LOAD(W, J, H) do { _Pragma("unroll") for (int i = 0; i < 8; ++i) { const unsigned e = IDX16[(F.wave * 8 + (J)) * 128 + 64 * (H) + 8 * g + i]; W[i] = *(const GAS v4u*)(eb + (e * 2048u + lo)); } } while (0)
; DI void p9v2_phase(Frame& F) {
;     ...
;             P9A_LOAD(wA, 0, 0);
; #pragma unroll
;             for (int j = 0; j < 8; ++j) {
;                 P9A_LOAD(wB, j, 1);
;                 P9A_COMP(wA, j, 0);
;                 if (j < 7) P9A_LOAD(wA, j + 1, 0);
;                 P9A_COMP(wB, j, 1);
;             }
	v_lshlrev_b32_sdwa v3, v198, v25 dst_sel:DWORD dst_unused:UNUSED_PAD src0_sel:DWORD src1_sel:WORD_1
	v_lshlrev_b32_sdwa v4, v198, v25 dst_sel:DWORD dst_unused:UNUSED_PAD src0_sel:DWORD src1_sel:WORD_0
	v_or_b32_e32 v3, v3, v1
	v_or_b32_e32 v4, v4, v130
	global_load_dwordx4 v[30:33], v3, s[46:47]
	global_load_dwordx4 v[34:37], v4, s[46:47]
	v_lshlrev_b32_sdwa v3, v198, v24 dst_sel:DWORD dst_unused:UNUSED_PAD src0_sel:DWORD src1_sel:WORD_1
	v_lshlrev_b32_sdwa v4, v198, v24 dst_sel:DWORD dst_unused:UNUSED_PAD src0_sel:DWORD src1_sel:WORD_0
	v_or_b32_e32 v3, v3, v1
	v_or_b32_e32 v4, v4, v130
	global_load_dwordx4 v[38:41], v3, s[46:47]
	global_load_dwordx4 v[42:45], v4, s[46:47]
	v_lshlrev_b32_sdwa v3, v198, v23 dst_sel:DWORD dst_unused:UNUSED_PAD src0_sel:DWORD src1_sel:WORD_1
	v_lshlrev_b32_sdwa v4, v198, v23 dst_sel:DWORD dst_unused:UNUSED_PAD src0_sel:DWORD src1_sel:WORD_0
	v_or_b32_e32 v3, v3, v1
	v_or_b32_e32 v4, v4, v130
	global_load_dwordx4 v[46:49], v3, s[46:47]
	global_load_dwordx4 v[50:53], v4, s[46:47]
	v_lshlrev_b32_sdwa v3, v198, v22 dst_sel:DWORD dst_unused:UNUSED_PAD src0_sel:DWORD src1_sel:WORD_1
	v_lshlrev_b32_sdwa v4, v198, v22 dst_sel:DWORD dst_unused:UNUSED_PAD src0_sel:DWORD src1_sel:WORD_0
	v_or_b32_e32 v3, v3, v1
	ds_read_b128 v[22:25], v2 offset:4096
	v_or_b32_e32 v4, v4, v130
	global_load_dwordx4 v[54:57], v3, s[46:47]
	global_load_dwordx4 v[58:61], v4, s[46:47]
	v_mov_b32_e32 v3, 0
	v_mov_b32_e32 v4, 0
	s_waitcnt vmcnt(15) lgkmcnt(0)
	v_dot4c_i32_i8_e32 v3, v22, v26
	v_dot4c_i32_i8_e32 v3, v23, v27
	v_mov_b32_e32 v27, 0
	s_waitcnt vmcnt(11)
	v_dot4c_i32_i8_e32 v27, v22, v74
	v_dot4c_i32_i8_e32 v27, v23, v75
	v_dot4c_i32_i8_e32 v3, v24, v28
	v_dot4c_i32_i8_e32 v27, v24, v76
	v_dot4c_i32_i8_e32 v3, v25, v29
	v_dot4c_i32_i8_e32 v4, v22, v62
	v_mov_b32_e32 v5, 0
	v_mov_b32_e32 v26, 0
	v_dot4c_i32_i8_e32 v27, v25, v77
	v_mov_b32_e32 v28, 0
	v_mov_b32_e32 v29, 0
	v_mov_b32_e32 v62, 0
	v_dot4c_i32_i8_e32 v5, v22, v66
	v_dot4c_i32_i8_e32 v26, v22, v70
	s_waitcnt vmcnt(10)
	v_dot4c_i32_i8_e32 v28, v22, v78
	s_waitcnt vmcnt(9)
	v_dot4c_i32_i8_e32 v29, v22, v82
	s_waitcnt vmcnt(8)
	v_dot4c_i32_i8_e32 v62, v22, v86
	v_cndmask_b32_e64 v22, v3, v27, s[2:3]
	ds_bpermute_b32 v22, v159, v22
	v_dot4c_i32_i8_e32 v4, v23, v63
	v_dot4c_i32_i8_e32 v28, v23, v79
	v_dot4c_i32_i8_e32 v4, v24, v64
	v_dot4c_i32_i8_e32 v5, v23, v67
	v_dot4c_i32_i8_e32 v26, v23, v71
	v_dot4c_i32_i8_e32 v28, v24, v80
	v_dot4c_i32_i8_e32 v29, v23, v83
	v_dot4c_i32_i8_e32 v62, v23, v87
	v_dot4c_i32_i8_e32 v4, v25, v65
	v_dot4c_i32_i8_e32 v5, v24, v68
	v_dot4c_i32_i8_e32 v26, v24, v72
	v_dot4c_i32_i8_e32 v28, v25, v81
	v_dot4c_i32_i8_e32 v29, v24, v84
	v_dot4c_i32_i8_e32 v62, v24, v88
	v_cndmask_b32_e64 v3, v27, v3, s[2:3]
	v_dot4c_i32_i8_e32 v5, v25, v69
	v_dot4c_i32_i8_e32 v26, v25, v73
	v_dot4c_i32_i8_e32 v29, v25, v85
	v_dot4c_i32_i8_e32 v62, v25, v89
	s_waitcnt lgkmcnt(0)
	v_add_u32_e32 v3, v3, v22
	v_cndmask_b32_e64 v22, v28, v4, s[2:3]
	v_cndmask_b32_e64 v4, v4, v28, s[2:3]
	ds_bpermute_b32 v4, v159, v4
	v_cndmask_b32_e64 v23, v5, v29, s[2:3]
	v_cndmask_b32_e64 v24, v26, v62, s[2:3]
	ds_bpermute_b32 v23, v159, v23
	ds_bpermute_b32 v24, v159, v24
	s_waitcnt lgkmcnt(2)
	v_add_u32_e32 v4, v22, v4
	v_cndmask_b32_e64 v5, v29, v5, s[2:3]
	v_cndmask_b32_e64 v22, v62, v26, s[2:3]
	s_waitcnt lgkmcnt(1)
	v_add_u32_e32 v5, v5, v23
	s_waitcnt lgkmcnt(0)
	v_add_u32_e32 v26, v22, v24
	ds_read_b128 v[22:25], v181 offset:896
	v_cndmask_b32_e64 v27, v5, v3, s[4:5]
	v_cndmask_b32_e64 v3, v3, v5, s[4:5]
	ds_bpermute_b32 v3, v160, v3
	v_cndmask_b32_e64 v5, v4, v26, s[4:5]
	v_cndmask_b32_e64 v4, v26, v4, s[4:5]
	s_waitcnt lgkmcnt(1)
	v_lshlrev_b32_sdwa v26, v198, v22 dst_sel:DWORD dst_unused:UNUSED_PAD src0_sel:DWORD src1_sel:WORD_1
	v_lshlrev_b32_sdwa v22, v198, v22 dst_sel:DWORD dst_unused:UNUSED_PAD src0_sel:DWORD src1_sel:WORD_0
	v_or_b32_e32 v62, v26, v1
	v_or_b32_e32 v22, v22, v130
	s_waitcnt lgkmcnt(0)
	v_add_u32_e32 v3, v27, v3
	global_load_dwordx4 v[26:29], v22, s[46:47]
	s_nop 0
	global_load_dwordx4 v[62:65], v62, s[46:47]
	v_lshlrev_b32_sdwa v22, v198, v23 dst_sel:DWORD dst_unused:UNUSED_PAD src0_sel:DWORD src1_sel:WORD_1
	v_lshlrev_b32_sdwa v23, v198, v23 dst_sel:DWORD dst_unused:UNUSED_PAD src0_sel:DWORD src1_sel:WORD_0
	v_or_b32_e32 v22, v22, v1
	v_or_b32_e32 v23, v23, v130
	global_load_dwordx4 v[66:69], v23, s[46:47]
	global_load_dwordx4 v[70:73], v22, s[46:47]
	v_lshlrev_b32_sdwa v22, v198, v24 dst_sel:DWORD dst_unused:UNUSED_PAD src0_sel:DWORD src1_sel:WORD_1
	v_lshlrev_b32_sdwa v23, v198, v24 dst_sel:DWORD dst_unused:UNUSED_PAD src0_sel:DWORD src1_sel:WORD_0
	v_or_b32_e32 v22, v22, v1
	v_or_b32_e32 v23, v23, v130
	global_load_dwordx4 v[74:77], v23, s[46:47]
	global_load_dwordx4 v[78:81], v22, s[46:47]
	v_lshlrev_b32_sdwa v22, v198, v25 dst_sel:DWORD dst_unused:UNUSED_PAD src0_sel:DWORD src1_sel:WORD_1
	v_lshlrev_b32_sdwa v82, v198, v25 dst_sel:DWORD dst_unused:UNUSED_PAD src0_sel:DWORD src1_sel:WORD_0
	v_or_b32_e32 v86, v22, v1
	ds_read_b128 v[22:25], v2 offset:6144
	v_mov_b32_e32 v90, 0
	v_or_b32_e32 v82, v82, v130
	global_load_dwordx4 v[82:85], v82, s[46:47]
	s_nop 0
	global_load_dwordx4 v[86:89], v86, s[46:47]
	ds_bpermute_b32 v5, v160, v5
	s_waitcnt vmcnt(8) lgkmcnt(1)
; #define P9A_LOAD(W, J, H) do { _Pragma("unroll") for (int i = 0; i < 8; ++i) { const unsigned e = IDX16[(F.wave * 8 + (J)) * 128 + 64 * (H) + 8 * g + i]; W[i] = *(const GAS v4u*)(eb + (e * 2048u + lo)); } } while (0)
; DI void p9v2_phase(Frame& F) {
;     ...
;             P9A_LOAD(wA, 0, 0);
; #pragma unroll
;             for (int j = 0; j < 8; ++j) {
;                 P9A_LOAD(wB, j, 1);
;                 P9A_COMP(wA, j, 0);
;                 if (j < 7) P9A_LOAD(wA, j + 1, 0);
;                 P9A_COMP(wB, j, 1);
;             }
	v_dot4c_i32_i8_e32 v90, v22, v58
	v_mov_b32_e32 v58, 0
	v_dot4c_i32_i8_e32 v58, v22, v54
	v_mov_b32_e32 v54, 0
	v_dot4c_i32_i8_e32 v54, v22, v50
	v_mov_b32_e32 v50, 0
	v_dot4c_i32_i8_e32 v50, v22, v46
	v_mov_b32_e32 v46, 0
	v_dot4c_i32_i8_e32 v46, v22, v42
	v_mov_b32_e32 v42, 0
	v_dot4c_i32_i8_e32 v90, v23, v59
	v_dot4c_i32_i8_e32 v46, v23, v43
	v_dot4c_i32_i8_e32 v42, v22, v38
	v_mov_b32_e32 v38, 0
	v_dot4c_i32_i8_e32 v90, v24, v60
	v_dot4c_i32_i8_e32 v58, v23, v55
	v_dot4c_i32_i8_e32 v46, v24, v44
	v_dot4c_i32_i8_e32 v42, v23, v39
	v_dot4c_i32_i8_e32 v38, v22, v34
	v_mov_b32_e32 v34, 0
	v_dot4c_i32_i8_e32 v90, v25, v61
	v_dot4c_i32_i8_e32 v58, v24, v56
	v_dot4c_i32_i8_e32 v54, v23, v51
	v_dot4c_i32_i8_e32 v46, v25, v45
	v_dot4c_i32_i8_e32 v42, v24, v40
	v_dot4c_i32_i8_e32 v38, v23, v35
	v_dot4c_i32_i8_e32 v34, v22, v30
	v_dot4c_i32_i8_e32 v58, v25, v57
	v_dot4c_i32_i8_e32 v54, v24, v52
	v_dot4c_i32_i8_e32 v50, v23, v47
	v_dot4c_i32_i8_e32 v42, v25, v41
	v_dot4c_i32_i8_e32 v38, v24, v36
	v_cndmask_b32_e64 v22, v90, v46, s[2:3]
	v_dot4c_i32_i8_e32 v34, v23, v31
	v_dot4c_i32_i8_e32 v54, v25, v53
	v_dot4c_i32_i8_e32 v50, v24, v48
	v_dot4c_i32_i8_e32 v38, v25, v37
	ds_bpermute_b32 v22, v159, v22
	v_dot4c_i32_i8_e32 v34, v24, v32
	v_cndmask_b32_e64 v24, v58, v42, s[2:3]
	v_dot4c_i32_i8_e32 v50, v25, v49
	v_dot4c_i32_i8_e32 v34, v25, v33
	ds_bpermute_b32 v24, v159, v24
	v_cndmask_b32_e64 v25, v54, v38, s[2:3]
	ds_bpermute_b32 v25, v159, v25
	v_cndmask_b32_e64 v30, v50, v34, s[2:3]
	ds_bpermute_b32 v30, v159, v30
	v_cndmask_b32_e64 v23, v46, v90, s[2:3]
	s_waitcnt lgkmcnt(3)
	v_add_u32_e32 v22, v23, v22
	v_cndmask_b32_e64 v23, v42, v58, s[2:3]
	s_waitcnt lgkmcnt(2)
	v_add_u32_e32 v23, v23, v24
	v_cndmask_b32_e64 v24, v38, v54, s[2:3]
	s_waitcnt lgkmcnt(1)
	v_add_u32_e32 v24, v24, v25
	v_cndmask_b32_e64 v25, v34, v50, s[2:3]
	s_waitcnt lgkmcnt(0)
	v_add_u32_e32 v25, v25, v30
	v_cndmask_b32_e64 v30, v22, v24, s[4:5]
	ds_bpermute_b32 v30, v160, v30
	v_cndmask_b32_e64 v31, v23, v25, s[4:5]
	ds_bpermute_b32 v31, v160, v31
	v_cndmask_b32_e64 v22, v24, v22, s[4:5]
	v_add_u32_e32 v4, v4, v5
	s_waitcnt lgkmcnt(1)
	v_add_u32_e32 v30, v22, v30
	v_cndmask_b32_e64 v22, v25, v23, s[4:5]
	v_cndmask_b32_e64 v5, v3, v4, s[6:7]
	s_waitcnt lgkmcnt(0)
	v_add_u32_e32 v31, v22, v31
	ds_bpermute_b32 v5, v161, v5
	v_cndmask_b32_e64 v22, v30, v31, s[6:7]
	ds_bpermute_b32 v32, v161, v22
	ds_read_b128 v[22:25], v181 offset:1024
	v_cndmask_b32_e64 v3, v4, v3, s[6:7]
	s_waitcnt lgkmcnt(2)
	v_add3_u32 v11, v5, v11, v3
	v_cndmask_b32_e64 v3, v31, v30, s[6:7]
	s_waitcnt lgkmcnt(1)
	v_add3_u32 v12, v32, v12, v3
	s_waitcnt lgkmcnt(0)
	v_lshlrev_b32_sdwa v3, v198, v25 dst_sel:DWORD dst_unused:UNUSED_PAD src0_sel:DWORD src1_sel:WORD_1
	v_lshlrev_b32_sdwa v4, v198, v25 dst_sel:DWORD dst_unused:UNUSED_PAD src0_sel:DWORD src1_sel:WORD_0
	v_or_b32_e32 v3, v3, v1
	v_or_b32_e32 v4, v4, v130
	global_load_dwordx4 v[30:33], v3, s[46:47]
	global_load_dwordx4 v[34:37], v4, s[46:47]
	v_lshlrev_b32_sdwa v3, v198, v24 dst_sel:DWORD dst_unused:UNUSED_PAD src0_sel:DWORD src1_sel:WORD_1
	v_lshlrev_b32_sdwa v4, v198, v24 dst_sel:DWORD dst_unused:UNUSED_PAD src0_sel:DWORD src1_sel:WORD_0
	v_or_b32_e32 v3, v3, v1
	v_or_b32_e32 v4, v4, v130
	global_load_dwordx4 v[38:41], v3, s[46:47]
	global_load_dwordx4 v[42:45], v4, s[46:47]
	v_lshlrev_b32_sdwa v3, v198, v23 dst_sel:DWORD dst_unused:UNUSED_PAD src0_sel:DWORD src1_sel:WORD_1
	v_lshlrev_b32_sdwa v4, v198, v23 dst_sel:DWORD dst_unused:UNUSED_PAD src0_sel:DWORD src1_sel:WORD_0
	v_or_b32_e32 v3, v3, v1
	v_or_b32_e32 v4, v4, v130
	global_load_dwordx4 v[46:49], v3, s[46:47]
	global_load_dwordx4 v[50:53], v4, s[46:47]
	v_lshlrev_b32_sdwa v3, v198, v22 dst_sel:DWORD dst_unused:UNUSED_PAD src0_sel:DWORD src1_sel:WORD_1
	v_lshlrev_b32_sdwa v4, v198, v22 dst_sel:DWORD dst_unused:UNUSED_PAD src0_sel:DWORD src1_sel:WORD_0
	v_or_b32_e32 v3, v3, v1
	ds_read_b128 v[22:25], v2 offset:6144
	v_or_b32_e32 v4, v4, v130
	global_load_dwordx4 v[54:57], v3, s[46:47]
	global_load_dwordx4 v[58:61], v4, s[46:47]
	v_mov_b32_e32 v3, 0
	v_mov_b32_e32 v4, 0
	s_waitcnt vmcnt(15) lgkmcnt(0)
	v_dot4c_i32_i8_e32 v3, v22, v26
	v_dot4c_i32_i8_e32 v3, v23, v27
	v_mov_b32_e32 v27, 0
	s_waitcnt vmcnt(11)
	v_dot4c_i32_i8_e32 v27, v22, v74
	v_dot4c_i32_i8_e32 v27, v23, v75
	v_dot4c_i32_i8_e32 v3, v24, v28
	v_dot4c_i32_i8_e32 v27, v24, v76
	v_dot4c_i32_i8_e32 v3, v25, v29
	v_dot4c_i32_i8_e32 v4, v22, v62
	v_mov_b32_e32 v5, 0
	v_mov_b32_e32 v26, 0
	v_dot4c_i32_i8_e32 v27, v25, v77
	v_mov_b32_e32 v28, 0
	v_mov_b32_e32 v29, 0
	v_mov_b32_e32 v62, 0
	v_dot4c_i32_i8_e32 v5, v22, v66
	v_dot4c_i32_i8_e32 v26, v22, v70
	s_waitcnt vmcnt(10)
	v_dot4c_i32_i8_e32 v28, v22, v78
	s_waitcnt vmcnt(9)
	v_dot4c_i32_i8_e32 v29, v22, v82
	s_waitcnt vmcnt(8)
	v_dot4c_i32_i8_e32 v62, v22, v86
	v_cndmask_b32_e64 v22, v3, v27, s[2:3]
	ds_bpermute_b32 v22, v159, v22
	v_dot4c_i32_i8_e32 v4, v23, v63
	v_dot4c_i32_i8_e32 v28, v23, v79
	v_dot4c_i32_i8_e32 v4, v24, v64
	v_dot4c_i32_i8_e32 v5, v23, v67
	v_dot4c_i32_i8_e32 v26, v23, v71
	v_dot4c_i32_i8_e32 v28, v24, v80
	v_dot4c_i32_i8_e32 v29, v23, v83
	v_dot4c_i32_i8_e32 v62, v23, v87
	v_dot4c_i32_i8_e32 v4, v25, v65
	v_dot4c_i32_i8_e32 v5, v24, v68
	v_dot4c_i32_i8_e32 v26, v24, v72
	v_dot4c_i32_i8_e32 v28, v25, v81
	v_dot4c_i32_i8_e32 v29, v24, v84
	v_dot4c_i32_i8_e32 v62, v24, v88
	v_cndmask_b32_e64 v3, v27, v3, s[2:3]
	v_dot4c_i32_i8_e32 v5, v25, v69
	v_dot4c_i32_i8_e32 v26, v25, v73
	v_dot4c_i32_i8_e32 v29, v25, v85
	v_dot4c_i32_i8_e32 v62, v25, v89
	s_waitcnt lgkmcnt(0)
; #define P9A_LOAD(W, J, H) do { _Pragma("unroll") for (int i = 0; i < 8; ++i) { const unsigned e = IDX16[(F.wave * 8 + (J)) * 128 + 64 * (H) + 8 * g + i]; W[i] = *(const GAS v4u*)(eb + (e * 2048u + lo)); } } while (0)
; DI void p9v2_phase(Frame& F) {
;     ...
;             P9A_LOAD(wA, 0, 0);
; #pragma unroll
;             for (int j = 0; j < 8; ++j) {
;                 P9A_LOAD(wB, j, 1);
;                 P9A_COMP(wA, j, 0);
;                 if (j < 7) P9A_LOAD(wA, j + 1, 0);
;                 P9A_COMP(wB, j, 1);
;             }
	v_add_u32_e32 v3, v3, v22
	v_cndmask_b32_e64 v22, v28, v4, s[2:3]
	v_cndmask_b32_e64 v4, v4, v28, s[2:3]
	ds_bpermute_b32 v4, v159, v4
	v_cndmask_b32_e64 v23, v5, v29, s[2:3]
	v_cndmask_b32_e64 v24, v26, v62, s[2:3]
	ds_bpermute_b32 v23, v159, v23
	ds_bpermute_b32 v24, v159, v24
	s_waitcnt lgkmcnt(2)
	v_add_u32_e32 v4, v22, v4
	v_cndmask_b32_e64 v5, v29, v5, s[2:3]
	v_cndmask_b32_e64 v22, v62, v26, s[2:3]
	s_waitcnt lgkmcnt(1)
	v_add_u32_e32 v5, v5, v23
	s_waitcnt lgkmcnt(0)
	v_add_u32_e32 v26, v22, v24
	ds_read_b128 v[22:25], v181 offset:1152
	v_cndmask_b32_e64 v27, v5, v3, s[4:5]
	v_cndmask_b32_e64 v3, v3, v5, s[4:5]
	ds_bpermute_b32 v3, v160, v3
	v_cndmask_b32_e64 v5, v4, v26, s[4:5]
	v_cndmask_b32_e64 v4, v26, v4, s[4:5]
	s_waitcnt lgkmcnt(1)
	v_lshlrev_b32_sdwa v26, v198, v22 dst_sel:DWORD dst_unused:UNUSED_PAD src0_sel:DWORD src1_sel:WORD_1
	v_lshlrev_b32_sdwa v22, v198, v22 dst_sel:DWORD dst_unused:UNUSED_PAD src0_sel:DWORD src1_sel:WORD_0
	v_or_b32_e32 v62, v26, v1
	v_or_b32_e32 v22, v22, v130
	s_waitcnt lgkmcnt(0)
	v_add_u32_e32 v3, v27, v3
	global_load_dwordx4 v[26:29], v22, s[46:47]
	s_nop 0
	global_load_dwordx4 v[62:65], v62, s[46:47]
	v_lshlrev_b32_sdwa v22, v198, v23 dst_sel:DWORD dst_unused:UNUSED_PAD src0_sel:DWORD src1_sel:WORD_1
	v_lshlrev_b32_sdwa v23, v198, v23 dst_sel:DWORD dst_unused:UNUSED_PAD src0_sel:DWORD src1_sel:WORD_0
	v_or_b32_e32 v23, v23, v130
	v_or_b32_e32 v22, v22, v1
	global_load_dwordx4 v[66:69], v23, s[46:47]
	global_load_dwordx4 v[70:73], v22, s[46:47]
	v_lshlrev_b32_sdwa v23, v198, v24 dst_sel:DWORD dst_unused:UNUSED_PAD src0_sel:DWORD src1_sel:WORD_0
	v_lshlrev_b32_sdwa v22, v198, v24 dst_sel:DWORD dst_unused:UNUSED_PAD src0_sel:DWORD src1_sel:WORD_1
	v_or_b32_e32 v23, v23, v130
	v_or_b32_e32 v22, v22, v1
	global_load_dwordx4 v[74:77], v23, s[46:47]
	global_load_dwordx4 v[78:81], v22, s[46:47]
	v_lshlrev_b32_sdwa v22, v198, v25 dst_sel:DWORD dst_unused:UNUSED_PAD src0_sel:DWORD src1_sel:WORD_1
	v_lshlrev_b32_sdwa v82, v198, v25 dst_sel:DWORD dst_unused:UNUSED_PAD src0_sel:DWORD src1_sel:WORD_0
	v_or_b32_e32 v86, v22, v1
	v_or_b32_e32 v82, v82, v130
	ds_read_b128 v[22:25], v2 offset:8192
	global_load_dwordx4 v[82:85], v82, s[46:47]
	s_nop 0
	global_load_dwordx4 v[86:89], v86, s[46:47]
	v_mov_b32_e32 v90, 0
	ds_bpermute_b32 v5, v160, v5
	s_waitcnt vmcnt(8) lgkmcnt(1)
	v_dot4c_i32_i8_e32 v90, v22, v58
	v_mov_b32_e32 v58, 0
	v_dot4c_i32_i8_e32 v58, v22, v54
	v_mov_b32_e32 v54, 0
	v_dot4c_i32_i8_e32 v54, v22, v50
	v_mov_b32_e32 v50, 0
	v_dot4c_i32_i8_e32 v50, v22, v46
	v_mov_b32_e32 v46, 0
	v_dot4c_i32_i8_e32 v46, v22, v42
	v_mov_b32_e32 v42, 0
	v_dot4c_i32_i8_e32 v90, v23, v59
	v_dot4c_i32_i8_e32 v46, v23, v43
	v_dot4c_i32_i8_e32 v42, v22, v38
	v_mov_b32_e32 v38, 0
	v_dot4c_i32_i8_e32 v90, v24, v60
	v_dot4c_i32_i8_e32 v58, v23, v55
	v_dot4c_i32_i8_e32 v46, v24, v44
	v_dot4c_i32_i8_e32 v42, v23, v39
	v_dot4c_i32_i8_e32 v38, v22, v34
	v_mov_b32_e32 v34, 0
	v_dot4c_i32_i8_e32 v90, v25, v61
	v_dot4c_i32_i8_e32 v58, v24, v56
	v_dot4c_i32_i8_e32 v54, v23, v51
	v_dot4c_i32_i8_e32 v46, v25, v45
	v_dot4c_i32_i8_e32 v42, v24, v40
	v_dot4c_i32_i8_e32 v38, v23, v35
	v_dot4c_i32_i8_e32 v34, v22, v30
	v_dot4c_i32_i8_e32 v58, v25, v57
	v_dot4c_i32_i8_e32 v54, v24, v52
	v_dot4c_i32_i8_e32 v50, v23, v47
	v_dot4c_i32_i8_e32 v42, v25, v41
	v_dot4c_i32_i8_e32 v38, v24, v36
	v_cndmask_b32_e64 v22, v90, v46, s[2:3]
	v_dot4c_i32_i8_e32 v34, v23, v31
	v_dot4c_i32_i8_e32 v54, v25, v53
	v_dot4c_i32_i8_e32 v50, v24, v48
	v_dot4c_i32_i8_e32 v38, v25, v37
	ds_bpermute_b32 v22, v159, v22
	v_dot4c_i32_i8_e32 v34, v24, v32
	v_cndmask_b32_e64 v24, v58, v42, s[2:3]
	v_dot4c_i32_i8_e32 v50, v25, v49
	v_dot4c_i32_i8_e32 v34, v25, v33
	ds_bpermute_b32 v24, v159, v24
	v_cndmask_b32_e64 v25, v54, v38, s[2:3]
	ds_bpermute_b32 v25, v159, v25
	v_cndmask_b32_e64 v30, v50, v34, s[2:3]
	ds_bpermute_b32 v30, v159, v30
	v_cndmask_b32_e64 v23, v46, v90, s[2:3]
	s_waitcnt lgkmcnt(3)
	v_add_u32_e32 v22, v23, v22
	v_cndmask_b32_e64 v23, v42, v58, s[2:3]
	s_waitcnt lgkmcnt(2)
	v_add_u32_e32 v23, v23, v24
	v_cndmask_b32_e64 v24, v38, v54, s[2:3]
	s_waitcnt lgkmcnt(1)
	v_add_u32_e32 v24, v24, v25
	v_cndmask_b32_e64 v25, v34, v50, s[2:3]
	s_waitcnt lgkmcnt(0)
	v_add_u32_e32 v25, v25, v30
	v_cndmask_b32_e64 v30, v22, v24, s[4:5]
	ds_bpermute_b32 v30, v160, v30
	v_cndmask_b32_e64 v31, v23, v25, s[4:5]
	ds_bpermute_b32 v31, v160, v31
	v_cndmask_b32_e64 v22, v24, v22, s[4:5]
	v_add_u32_e32 v4, v4, v5
	s_waitcnt lgkmcnt(1)
	v_add_u32_e32 v30, v22, v30
	v_cndmask_b32_e64 v22, v25, v23, s[4:5]
	v_cndmask_b32_e64 v5, v3, v4, s[6:7]
	s_waitcnt lgkmcnt(0)
	v_add_u32_e32 v31, v22, v31
	ds_bpermute_b32 v5, v161, v5
	v_cndmask_b32_e64 v22, v30, v31, s[6:7]
	ds_bpermute_b32 v32, v161, v22
	ds_read_b128 v[22:25], v181 offset:1280
	v_cndmask_b32_e64 v3, v4, v3, s[6:7]
	s_waitcnt lgkmcnt(2)
	v_add3_u32 v13, v5, v13, v3
	v_cndmask_b32_e64 v3, v31, v30, s[6:7]
	s_waitcnt lgkmcnt(1)
	v_add3_u32 v14, v32, v14, v3
	s_waitcnt lgkmcnt(0)
; #define P9A_LOAD(W, J, H) do { _Pragma("unroll") for (int i = 0; i < 8; ++i) { const unsigned e = IDX16[(F.wave * 8 + (J)) * 128 + 64 * (H) + 8 * g + i]; W[i] = *(const GAS v4u*)(eb + (e * 2048u + lo)); } } while (0)
; DI void p9v2_phase(Frame& F) {
;     ...
;             P9A_LOAD(wA, 0, 0);
; #pragma unroll
;             for (int j = 0; j < 8; ++j) {
;                 P9A_LOAD(wB, j, 1);
;                 P9A_COMP(wA, j, 0);
;                 if (j < 7) P9A_LOAD(wA, j + 1, 0);
;                 P9A_COMP(wB, j, 1);
;             }
	v_lshlrev_b32_sdwa v3, v198, v25 dst_sel:DWORD dst_unused:UNUSED_PAD src0_sel:DWORD src1_sel:WORD_1
	v_lshlrev_b32_sdwa v4, v198, v25 dst_sel:DWORD dst_unused:UNUSED_PAD src0_sel:DWORD src1_sel:WORD_0
	v_or_b32_e32 v3, v3, v1
	v_or_b32_e32 v4, v4, v130
	global_load_dwordx4 v[30:33], v3, s[46:47]
	global_load_dwordx4 v[34:37], v4, s[46:47]
	v_lshlrev_b32_sdwa v3, v198, v24 dst_sel:DWORD dst_unused:UNUSED_PAD src0_sel:DWORD src1_sel:WORD_1
	v_lshlrev_b32_sdwa v4, v198, v24 dst_sel:DWORD dst_unused:UNUSED_PAD src0_sel:DWORD src1_sel:WORD_0
	v_or_b32_e32 v3, v3, v1
	v_or_b32_e32 v4, v4, v130
	global_load_dwordx4 v[38:41], v3, s[46:47]
	global_load_dwordx4 v[42:45], v4, s[46:47]
	v_lshlrev_b32_sdwa v3, v198, v23 dst_sel:DWORD dst_unused:UNUSED_PAD src0_sel:DWORD src1_sel:WORD_1
	v_lshlrev_b32_sdwa v4, v198, v23 dst_sel:DWORD dst_unused:UNUSED_PAD src0_sel:DWORD src1_sel:WORD_0
	v_or_b32_e32 v3, v3, v1
	v_or_b32_e32 v4, v4, v130
	global_load_dwordx4 v[46:49], v3, s[46:47]
	global_load_dwordx4 v[50:53], v4, s[46:47]
	v_lshlrev_b32_sdwa v3, v198, v22 dst_sel:DWORD dst_unused:UNUSED_PAD src0_sel:DWORD src1_sel:WORD_1
	v_lshlrev_b32_sdwa v4, v198, v22 dst_sel:DWORD dst_unused:UNUSED_PAD src0_sel:DWORD src1_sel:WORD_0
	v_or_b32_e32 v3, v3, v1
	ds_read_b128 v[22:25], v2 offset:8192
	v_or_b32_e32 v4, v4, v130
	global_load_dwordx4 v[54:57], v3, s[46:47]
	global_load_dwordx4 v[58:61], v4, s[46:47]
	v_mov_b32_e32 v3, 0
	v_mov_b32_e32 v4, 0
	s_waitcnt vmcnt(15) lgkmcnt(0)
	v_dot4c_i32_i8_e32 v3, v22, v26
	v_dot4c_i32_i8_e32 v3, v23, v27
	v_mov_b32_e32 v27, 0
	s_waitcnt vmcnt(11)
	v_dot4c_i32_i8_e32 v27, v22, v74
	v_dot4c_i32_i8_e32 v27, v23, v75
	v_dot4c_i32_i8_e32 v3, v24, v28
	v_dot4c_i32_i8_e32 v27, v24, v76
	v_dot4c_i32_i8_e32 v3, v25, v29
	v_dot4c_i32_i8_e32 v4, v22, v62
	v_mov_b32_e32 v5, 0
	v_mov_b32_e32 v26, 0
	v_dot4c_i32_i8_e32 v27, v25, v77
	v_mov_b32_e32 v28, 0
	v_mov_b32_e32 v29, 0
	v_mov_b32_e32 v62, 0
	v_dot4c_i32_i8_e32 v5, v22, v66
	v_dot4c_i32_i8_e32 v26, v22, v70
	s_waitcnt vmcnt(10)
	v_dot4c_i32_i8_e32 v28, v22, v78
	s_waitcnt vmcnt(9)
	v_dot4c_i32_i8_e32 v29, v22, v82
	s_waitcnt vmcnt(8)
	v_dot4c_i32_i8_e32 v62, v22, v86
	v_cndmask_b32_e64 v22, v3, v27, s[2:3]
	ds_bpermute_b32 v22, v159, v22
	v_dot4c_i32_i8_e32 v4, v23, v63
	v_dot4c_i32_i8_e32 v28, v23, v79
	v_dot4c_i32_i8_e32 v4, v24, v64
	v_dot4c_i32_i8_e32 v5, v23, v67
	v_dot4c_i32_i8_e32 v26, v23, v71
	v_dot4c_i32_i8_e32 v28, v24, v80
	v_dot4c_i32_i8_e32 v29, v23, v83
	v_dot4c_i32_i8_e32 v62, v23, v87
	v_dot4c_i32_i8_e32 v4, v25, v65
	v_dot4c_i32_i8_e32 v5, v24, v68
	v_dot4c_i32_i8_e32 v26, v24, v72
	v_dot4c_i32_i8_e32 v28, v25, v81
	v_dot4c_i32_i8_e32 v29, v24, v84
	v_dot4c_i32_i8_e32 v62, v24, v88
	v_cndmask_b32_e64 v3, v27, v3, s[2:3]
	v_dot4c_i32_i8_e32 v5, v25, v69
	v_dot4c_i32_i8_e32 v26, v25, v73
	v_dot4c_i32_i8_e32 v29, v25, v85
	v_dot4c_i32_i8_e32 v62, v25, v89
	s_waitcnt lgkmcnt(0)
	v_add_u32_e32 v3, v3, v22
	v_cndmask_b32_e64 v22, v28, v4, s[2:3]
	v_cndmask_b32_e64 v4, v4, v28, s[2:3]
	ds_bpermute_b32 v4, v159, v4
	v_cndmask_b32_e64 v23, v5, v29, s[2:3]
	v_cndmask_b32_e64 v24, v26, v62, s[2:3]
	ds_bpermute_b32 v23, v159, v23
	ds_bpermute_b32 v24, v159, v24
	s_waitcnt lgkmcnt(2)
	v_add_u32_e32 v4, v22, v4
	v_cndmask_b32_e64 v5, v29, v5, s[2:3]
	v_cndmask_b32_e64 v22, v62, v26, s[2:3]
	s_waitcnt lgkmcnt(1)
	v_add_u32_e32 v5, v5, v23
	s_waitcnt lgkmcnt(0)
	v_add_u32_e32 v26, v22, v24
	ds_read_b128 v[22:25], v181 offset:1408
	v_cndmask_b32_e64 v27, v5, v3, s[4:5]
	v_cndmask_b32_e64 v3, v3, v5, s[4:5]
	ds_bpermute_b32 v3, v160, v3
	v_cndmask_b32_e64 v5, v4, v26, s[4:5]
	v_cndmask_b32_e64 v4, v26, v4, s[4:5]
	s_waitcnt lgkmcnt(1)
	v_lshlrev_b32_sdwa v26, v198, v22 dst_sel:DWORD dst_unused:UNUSED_PAD src0_sel:DWORD src1_sel:WORD_1
	v_lshlrev_b32_sdwa v22, v198, v22 dst_sel:DWORD dst_unused:UNUSED_PAD src0_sel:DWORD src1_sel:WORD_0
	v_or_b32_e32 v62, v26, v1
	v_or_b32_e32 v22, v22, v130
	s_waitcnt lgkmcnt(0)
	v_add_u32_e32 v3, v27, v3
	global_load_dwordx4 v[26:29], v22, s[46:47]
	s_nop 0
	global_load_dwordx4 v[62:65], v62, s[46:47]
	v_lshlrev_b32_sdwa v22, v198, v23 dst_sel:DWORD dst_unused:UNUSED_PAD src0_sel:DWORD src1_sel:WORD_1
	v_lshlrev_b32_sdwa v23, v198, v23 dst_sel:DWORD dst_unused:UNUSED_PAD src0_sel:DWORD src1_sel:WORD_0
	v_or_b32_e32 v23, v23, v130
	v_or_b32_e32 v22, v22, v1
	global_load_dwordx4 v[66:69], v23, s[46:47]
	global_load_dwordx4 v[70:73], v22, s[46:47]
	v_lshlrev_b32_sdwa v23, v198, v24 dst_sel:DWORD dst_unused:UNUSED_PAD src0_sel:DWORD src1_sel:WORD_0
	v_lshlrev_b32_sdwa v22, v198, v24 dst_sel:DWORD dst_unused:UNUSED_PAD src0_sel:DWORD src1_sel:WORD_1
	v_or_b32_e32 v23, v23, v130
	v_or_b32_e32 v22, v22, v1
	global_load_dwordx4 v[74:77], v23, s[46:47]
	global_load_dwordx4 v[78:81], v22, s[46:47]
	v_lshlrev_b32_sdwa v22, v198, v25 dst_sel:DWORD dst_unused:UNUSED_PAD src0_sel:DWORD src1_sel:WORD_1
	v_lshlrev_b32_sdwa v82, v198, v25 dst_sel:DWORD dst_unused:UNUSED_PAD src0_sel:DWORD src1_sel:WORD_0
	v_or_b32_e32 v86, v22, v1
	v_or_b32_e32 v82, v82, v130
	ds_read_b128 v[22:25], v2 offset:10240
	global_load_dwordx4 v[82:85], v82, s[46:47]
	s_nop 0
	global_load_dwordx4 v[86:89], v86, s[46:47]
	v_mov_b32_e32 v90, 0
	ds_bpermute_b32 v5, v160, v5
	s_waitcnt vmcnt(8) lgkmcnt(1)
; #define P9A_LOAD(W, J, H) do { _Pragma("unroll") for (int i = 0; i < 8; ++i) { const unsigned e = IDX16[(F.wave * 8 + (J)) * 128 + 64 * (H) + 8 * g + i]; W[i] = *(const GAS v4u*)(eb + (e * 2048u + lo)); } } while (0)
; DI void p9v2_phase(Frame& F) {
;     ...
;             P9A_LOAD(wA, 0, 0);
; #pragma unroll
;             for (int j = 0; j < 8; ++j) {
;                 P9A_LOAD(wB, j, 1);
;                 P9A_COMP(wA, j, 0);
;                 if (j < 7) P9A_LOAD(wA, j + 1, 0);
;                 P9A_COMP(wB, j, 1);
;             }
	v_dot4c_i32_i8_e32 v90, v22, v58
	v_mov_b32_e32 v58, 0
	v_dot4c_i32_i8_e32 v58, v22, v54
	v_mov_b32_e32 v54, 0
	v_dot4c_i32_i8_e32 v54, v22, v50
	v_mov_b32_e32 v50, 0
	v_dot4c_i32_i8_e32 v50, v22, v46
	v_mov_b32_e32 v46, 0
	v_dot4c_i32_i8_e32 v46, v22, v42
	v_mov_b32_e32 v42, 0
	v_dot4c_i32_i8_e32 v90, v23, v59
	v_dot4c_i32_i8_e32 v46, v23, v43
	v_dot4c_i32_i8_e32 v42, v22, v38
	v_mov_b32_e32 v38, 0
	v_dot4c_i32_i8_e32 v90, v24, v60
	v_dot4c_i32_i8_e32 v58, v23, v55
	v_dot4c_i32_i8_e32 v46, v24, v44
	v_dot4c_i32_i8_e32 v42, v23, v39
	v_dot4c_i32_i8_e32 v38, v22, v34
	v_mov_b32_e32 v34, 0
	v_dot4c_i32_i8_e32 v90, v25, v61
	v_dot4c_i32_i8_e32 v58, v24, v56
	v_dot4c_i32_i8_e32 v54, v23, v51
	v_dot4c_i32_i8_e32 v46, v25, v45
	v_dot4c_i32_i8_e32 v42, v24, v40
	v_dot4c_i32_i8_e32 v38, v23, v35
	v_dot4c_i32_i8_e32 v34, v22, v30
	v_dot4c_i32_i8_e32 v58, v25, v57
	v_dot4c_i32_i8_e32 v54, v24, v52
	v_dot4c_i32_i8_e32 v50, v23, v47
	v_dot4c_i32_i8_e32 v42, v25, v41
	v_dot4c_i32_i8_e32 v38, v24, v36
	v_cndmask_b32_e64 v22, v90, v46, s[2:3]
	v_dot4c_i32_i8_e32 v34, v23, v31
	v_dot4c_i32_i8_e32 v54, v25, v53
	v_dot4c_i32_i8_e32 v50, v24, v48
	v_dot4c_i32_i8_e32 v38, v25, v37
	ds_bpermute_b32 v22, v159, v22
	v_dot4c_i32_i8_e32 v34, v24, v32
	v_cndmask_b32_e64 v24, v58, v42, s[2:3]
	v_dot4c_i32_i8_e32 v50, v25, v49
	v_dot4c_i32_i8_e32 v34, v25, v33
	ds_bpermute_b32 v24, v159, v24
	v_cndmask_b32_e64 v25, v54, v38, s[2:3]
	ds_bpermute_b32 v25, v159, v25
	v_cndmask_b32_e64 v30, v50, v34, s[2:3]
	ds_bpermute_b32 v30, v159, v30
	v_cndmask_b32_e64 v23, v46, v90, s[2:3]
	s_waitcnt lgkmcnt(3)
	v_add_u32_e32 v22, v23, v22
	v_cndmask_b32_e64 v23, v42, v58, s[2:3]
	s_waitcnt lgkmcnt(2)
	v_add_u32_e32 v23, v23, v24
	v_cndmask_b32_e64 v24, v38, v54, s[2:3]
	s_waitcnt lgkmcnt(1)
	v_add_u32_e32 v24, v24, v25
	v_cndmask_b32_e64 v25, v34, v50, s[2:3]
	s_waitcnt lgkmcnt(0)
	v_add_u32_e32 v25, v25, v30
	v_cndmask_b32_e64 v30, v22, v24, s[4:5]
	ds_bpermute_b32 v30, v160, v30
	v_cndmask_b32_e64 v31, v23, v25, s[4:5]
	ds_bpermute_b32 v31, v160, v31
	v_cndmask_b32_e64 v22, v24, v22, s[4:5]
	v_add_u32_e32 v4, v4, v5
	s_waitcnt lgkmcnt(1)
	v_add_u32_e32 v30, v22, v30
	v_cndmask_b32_e64 v22, v25, v23, s[4:5]
	v_cndmask_b32_e64 v5, v3, v4, s[6:7]
	s_waitcnt lgkmcnt(0)
	v_add_u32_e32 v31, v22, v31
	ds_bpermute_b32 v5, v161, v5
	v_cndmask_b32_e64 v22, v30, v31, s[6:7]
	ds_bpermute_b32 v32, v161, v22
	ds_read_b128 v[22:25], v181 offset:1536
	v_cndmask_b32_e64 v3, v4, v3, s[6:7]
	s_waitcnt lgkmcnt(2)
	v_add3_u32 v15, v5, v15, v3
	v_cndmask_b32_e64 v3, v31, v30, s[6:7]
	s_waitcnt lgkmcnt(1)
	v_add3_u32 v16, v32, v16, v3
	s_waitcnt lgkmcnt(0)
	v_lshlrev_b32_sdwa v3, v198, v25 dst_sel:DWORD dst_unused:UNUSED_PAD src0_sel:DWORD src1_sel:WORD_1
	v_lshlrev_b32_sdwa v4, v198, v25 dst_sel:DWORD dst_unused:UNUSED_PAD src0_sel:DWORD src1_sel:WORD_0
	v_or_b32_e32 v3, v3, v1
	v_or_b32_e32 v4, v4, v130
	global_load_dwordx4 v[30:33], v3, s[46:47]
	global_load_dwordx4 v[34:37], v4, s[46:47]
	v_lshlrev_b32_sdwa v3, v198, v24 dst_sel:DWORD dst_unused:UNUSED_PAD src0_sel:DWORD src1_sel:WORD_1
	v_lshlrev_b32_sdwa v4, v198, v24 dst_sel:DWORD dst_unused:UNUSED_PAD src0_sel:DWORD src1_sel:WORD_0
	v_or_b32_e32 v3, v3, v1
	v_or_b32_e32 v4, v4, v130
	global_load_dwordx4 v[38:41], v3, s[46:47]
	global_load_dwordx4 v[42:45], v4, s[46:47]
	v_lshlrev_b32_sdwa v3, v198, v23 dst_sel:DWORD dst_unused:UNUSED_PAD src0_sel:DWORD src1_sel:WORD_1
	v_lshlrev_b32_sdwa v4, v198, v23 dst_sel:DWORD dst_unused:UNUSED_PAD src0_sel:DWORD src1_sel:WORD_0
	v_or_b32_e32 v3, v3, v1
	v_or_b32_e32 v4, v4, v130
	global_load_dwordx4 v[46:49], v3, s[46:47]
	global_load_dwordx4 v[50:53], v4, s[46:47]
	v_lshlrev_b32_sdwa v3, v198, v22 dst_sel:DWORD dst_unused:UNUSED_PAD src0_sel:DWORD src1_sel:WORD_1
	v_lshlrev_b32_sdwa v4, v198, v22 dst_sel:DWORD dst_unused:UNUSED_PAD src0_sel:DWORD src1_sel:WORD_0
	v_or_b32_e32 v3, v3, v1
	ds_read_b128 v[22:25], v2 offset:10240
	v_or_b32_e32 v4, v4, v130
	global_load_dwordx4 v[54:57], v3, s[46:47]
	global_load_dwordx4 v[58:61], v4, s[46:47]
	v_mov_b32_e32 v3, 0
	v_mov_b32_e32 v4, 0
	s_waitcnt vmcnt(15) lgkmcnt(0)
	v_dot4c_i32_i8_e32 v3, v22, v26
	v_dot4c_i32_i8_e32 v3, v23, v27
	v_mov_b32_e32 v27, 0
	s_waitcnt vmcnt(11)
	v_dot4c_i32_i8_e32 v27, v22, v74
	v_dot4c_i32_i8_e32 v27, v23, v75
	v_dot4c_i32_i8_e32 v3, v24, v28
	v_dot4c_i32_i8_e32 v27, v24, v76
	v_dot4c_i32_i8_e32 v3, v25, v29
	v_dot4c_i32_i8_e32 v4, v22, v62
	v_mov_b32_e32 v5, 0
	v_mov_b32_e32 v26, 0
	v_dot4c_i32_i8_e32 v27, v25, v77
	v_mov_b32_e32 v28, 0
	v_mov_b32_e32 v29, 0
	v_mov_b32_e32 v62, 0
	v_dot4c_i32_i8_e32 v5, v22, v66
	v_dot4c_i32_i8_e32 v26, v22, v70
	s_waitcnt vmcnt(10)
	v_dot4c_i32_i8_e32 v28, v22, v78
	s_waitcnt vmcnt(9)
	v_dot4c_i32_i8_e32 v29, v22, v82
	s_waitcnt vmcnt(8)
	v_dot4c_i32_i8_e32 v62, v22, v86
	v_cndmask_b32_e64 v22, v3, v27, s[2:3]
	ds_bpermute_b32 v22, v159, v22
	v_dot4c_i32_i8_e32 v4, v23, v63
	v_dot4c_i32_i8_e32 v28, v23, v79
	v_dot4c_i32_i8_e32 v4, v24, v64
	v_dot4c_i32_i8_e32 v5, v23, v67
	v_dot4c_i32_i8_e32 v26, v23, v71
	v_dot4c_i32_i8_e32 v28, v24, v80
	v_dot4c_i32_i8_e32 v29, v23, v83
	v_dot4c_i32_i8_e32 v62, v23, v87
	v_dot4c_i32_i8_e32 v4, v25, v65
	v_dot4c_i32_i8_e32 v5, v24, v68
	v_dot4c_i32_i8_e32 v26, v24, v72
	v_dot4c_i32_i8_e32 v28, v25, v81
	v_dot4c_i32_i8_e32 v29, v24, v84
	v_dot4c_i32_i8_e32 v62, v24, v88
	v_cndmask_b32_e64 v3, v27, v3, s[2:3]
	v_dot4c_i32_i8_e32 v5, v25, v69
	v_dot4c_i32_i8_e32 v26, v25, v73
	v_dot4c_i32_i8_e32 v29, v25, v85
	v_dot4c_i32_i8_e32 v62, v25, v89
	s_waitcnt lgkmcnt(0)
; #define P9A_LOAD(W, J, H) do { _Pragma("unroll") for (int i = 0; i < 8; ++i) { const unsigned e = IDX16[(F.wave * 8 + (J)) * 128 + 64 * (H) + 8 * g + i]; W[i] = *(const GAS v4u*)(eb + (e * 2048u + lo)); } } while (0)
; DI void p9v2_phase(Frame& F) {
;     ...
;             P9A_LOAD(wA, 0, 0);
; #pragma unroll
;             for (int j = 0; j < 8; ++j) {
;                 P9A_LOAD(wB, j, 1);
;                 P9A_COMP(wA, j, 0);
;                 if (j < 7) P9A_LOAD(wA, j + 1, 0);
;                 P9A_COMP(wB, j, 1);
;             }
	v_add_u32_e32 v3, v3, v22
	v_cndmask_b32_e64 v22, v28, v4, s[2:3]
	v_cndmask_b32_e64 v4, v4, v28, s[2:3]
	ds_bpermute_b32 v4, v159, v4
	v_cndmask_b32_e64 v23, v5, v29, s[2:3]
	v_cndmask_b32_e64 v24, v26, v62, s[2:3]
	ds_bpermute_b32 v23, v159, v23
	ds_bpermute_b32 v24, v159, v24
	s_waitcnt lgkmcnt(2)
	v_add_u32_e32 v4, v22, v4
	v_cndmask_b32_e64 v5, v29, v5, s[2:3]
	v_cndmask_b32_e64 v22, v62, v26, s[2:3]
	s_waitcnt lgkmcnt(1)
	v_add_u32_e32 v5, v5, v23
	s_waitcnt lgkmcnt(0)
	v_add_u32_e32 v26, v22, v24
	ds_read_b128 v[22:25], v181 offset:1664
	v_cndmask_b32_e64 v27, v5, v3, s[4:5]
	v_cndmask_b32_e64 v3, v3, v5, s[4:5]
	ds_bpermute_b32 v3, v160, v3
	v_cndmask_b32_e64 v5, v4, v26, s[4:5]
	v_cndmask_b32_e64 v4, v26, v4, s[4:5]
	s_waitcnt lgkmcnt(1)
	v_lshlrev_b32_sdwa v26, v198, v22 dst_sel:DWORD dst_unused:UNUSED_PAD src0_sel:DWORD src1_sel:WORD_1
	v_lshlrev_b32_sdwa v22, v198, v22 dst_sel:DWORD dst_unused:UNUSED_PAD src0_sel:DWORD src1_sel:WORD_0
	v_or_b32_e32 v62, v26, v1
	v_or_b32_e32 v22, v22, v130
	s_waitcnt lgkmcnt(0)
	v_add_u32_e32 v3, v27, v3
	global_load_dwordx4 v[26:29], v22, s[46:47]
	s_nop 0
	global_load_dwordx4 v[62:65], v62, s[46:47]
	v_lshlrev_b32_sdwa v22, v198, v23 dst_sel:DWORD dst_unused:UNUSED_PAD src0_sel:DWORD src1_sel:WORD_1
	v_lshlrev_b32_sdwa v23, v198, v23 dst_sel:DWORD dst_unused:UNUSED_PAD src0_sel:DWORD src1_sel:WORD_0
	v_or_b32_e32 v23, v23, v130
	v_or_b32_e32 v22, v22, v1
	global_load_dwordx4 v[66:69], v23, s[46:47]
	global_load_dwordx4 v[70:73], v22, s[46:47]
	v_lshlrev_b32_sdwa v23, v198, v24 dst_sel:DWORD dst_unused:UNUSED_PAD src0_sel:DWORD src1_sel:WORD_0
	v_lshlrev_b32_sdwa v22, v198, v24 dst_sel:DWORD dst_unused:UNUSED_PAD src0_sel:DWORD src1_sel:WORD_1
	v_or_b32_e32 v23, v23, v130
	v_or_b32_e32 v22, v22, v1
	global_load_dwordx4 v[74:77], v23, s[46:47]
	global_load_dwordx4 v[78:81], v22, s[46:47]
	v_lshlrev_b32_sdwa v22, v198, v25 dst_sel:DWORD dst_unused:UNUSED_PAD src0_sel:DWORD src1_sel:WORD_1
	v_lshlrev_b32_sdwa v82, v198, v25 dst_sel:DWORD dst_unused:UNUSED_PAD src0_sel:DWORD src1_sel:WORD_0
	v_or_b32_e32 v86, v22, v1
	v_or_b32_e32 v82, v82, v130
	ds_read_b128 v[22:25], v2 offset:12288
	global_load_dwordx4 v[82:85], v82, s[46:47]
	s_nop 0
	global_load_dwordx4 v[86:89], v86, s[46:47]
	v_mov_b32_e32 v90, 0
	ds_bpermute_b32 v5, v160, v5
	s_waitcnt vmcnt(8) lgkmcnt(1)
	v_dot4c_i32_i8_e32 v90, v22, v58
	v_mov_b32_e32 v58, 0
	v_dot4c_i32_i8_e32 v58, v22, v54
	v_mov_b32_e32 v54, 0
	v_dot4c_i32_i8_e32 v54, v22, v50
	v_mov_b32_e32 v50, 0
	v_dot4c_i32_i8_e32 v50, v22, v46
	v_mov_b32_e32 v46, 0
	v_dot4c_i32_i8_e32 v46, v22, v42
	v_mov_b32_e32 v42, 0
	v_dot4c_i32_i8_e32 v90, v23, v59
	v_dot4c_i32_i8_e32 v46, v23, v43
	v_dot4c_i32_i8_e32 v42, v22, v38
	v_mov_b32_e32 v38, 0
	v_dot4c_i32_i8_e32 v90, v24, v60
	v_dot4c_i32_i8_e32 v58, v23, v55
	v_dot4c_i32_i8_e32 v46, v24, v44
	v_dot4c_i32_i8_e32 v42, v23, v39
	v_dot4c_i32_i8_e32 v38, v22, v34
	v_mov_b32_e32 v34, 0
	v_dot4c_i32_i8_e32 v90, v25, v61
	v_dot4c_i32_i8_e32 v58, v24, v56
	v_dot4c_i32_i8_e32 v54, v23, v51
	v_dot4c_i32_i8_e32 v46, v25, v45
	v_dot4c_i32_i8_e32 v42, v24, v40
	v_dot4c_i32_i8_e32 v38, v23, v35
	v_dot4c_i32_i8_e32 v34, v22, v30
	v_dot4c_i32_i8_e32 v58, v25, v57
	v_dot4c_i32_i8_e32 v54, v24, v52
	v_dot4c_i32_i8_e32 v50, v23, v47
	v_dot4c_i32_i8_e32 v42, v25, v41
	v_dot4c_i32_i8_e32 v38, v24, v36
	v_cndmask_b32_e64 v22, v90, v46, s[2:3]
	v_dot4c_i32_i8_e32 v34, v23, v31
	v_dot4c_i32_i8_e32 v54, v25, v53
	v_dot4c_i32_i8_e32 v50, v24, v48
	v_dot4c_i32_i8_e32 v38, v25, v37
	ds_bpermute_b32 v22, v159, v22
	v_dot4c_i32_i8_e32 v34, v24, v32
	v_cndmask_b32_e64 v24, v58, v42, s[2:3]
	v_dot4c_i32_i8_e32 v50, v25, v49
	v_dot4c_i32_i8_e32 v34, v25, v33
	ds_bpermute_b32 v24, v159, v24
	v_cndmask_b32_e64 v25, v54, v38, s[2:3]
	ds_bpermute_b32 v25, v159, v25
	v_cndmask_b32_e64 v30, v50, v34, s[2:3]
	ds_bpermute_b32 v30, v159, v30
	v_cndmask_b32_e64 v23, v46, v90, s[2:3]
	s_waitcnt lgkmcnt(3)
	v_add_u32_e32 v22, v23, v22
	v_cndmask_b32_e64 v23, v42, v58, s[2:3]
	s_waitcnt lgkmcnt(2)
	v_add_u32_e32 v23, v23, v24
	v_cndmask_b32_e64 v24, v38, v54, s[2:3]
	s_waitcnt lgkmcnt(1)
	v_add_u32_e32 v24, v24, v25
	v_cndmask_b32_e64 v25, v34, v50, s[2:3]
	s_waitcnt lgkmcnt(0)
	v_add_u32_e32 v25, v25, v30
	v_cndmask_b32_e64 v30, v22, v24, s[4:5]
	ds_bpermute_b32 v30, v160, v30
	v_cndmask_b32_e64 v31, v23, v25, s[4:5]
	ds_bpermute_b32 v31, v160, v31
	v_cndmask_b32_e64 v22, v24, v22, s[4:5]
	v_add_u32_e32 v4, v4, v5
	s_waitcnt lgkmcnt(1)
	v_add_u32_e32 v30, v22, v30
	v_cndmask_b32_e64 v22, v25, v23, s[4:5]
	v_cndmask_b32_e64 v5, v3, v4, s[6:7]
	s_waitcnt lgkmcnt(0)
	v_add_u32_e32 v31, v22, v31
	ds_bpermute_b32 v5, v161, v5
	v_cndmask_b32_e64 v22, v30, v31, s[6:7]
	ds_bpermute_b32 v32, v161, v22
	ds_read_b128 v[22:25], v181 offset:1792
	v_cndmask_b32_e64 v3, v4, v3, s[6:7]
	s_waitcnt lgkmcnt(2)
	v_add3_u32 v17, v5, v17, v3
	v_cndmask_b32_e64 v3, v31, v30, s[6:7]
	s_waitcnt lgkmcnt(1)
	v_add3_u32 v18, v32, v18, v3
	s_waitcnt lgkmcnt(0)
; #define P9A_LOAD(W, J, H) do { _Pragma("unroll") for (int i = 0; i < 8; ++i) { const unsigned e = IDX16[(F.wave * 8 + (J)) * 128 + 64 * (H) + 8 * g + i]; W[i] = *(const GAS v4u*)(eb + (e * 2048u + lo)); } } while (0)
; DI void p9v2_phase(Frame& F) {
;     ...
;             P9A_LOAD(wA, 0, 0);
; #pragma unroll
;             for (int j = 0; j < 8; ++j) {
;                 P9A_LOAD(wB, j, 1);
;                 P9A_COMP(wA, j, 0);
;                 if (j < 7) P9A_LOAD(wA, j + 1, 0);
;                 P9A_COMP(wB, j, 1);
;             }
	v_lshlrev_b32_sdwa v3, v198, v25 dst_sel:DWORD dst_unused:UNUSED_PAD src0_sel:DWORD src1_sel:WORD_1
	v_lshlrev_b32_sdwa v4, v198, v25 dst_sel:DWORD dst_unused:UNUSED_PAD src0_sel:DWORD src1_sel:WORD_0
	v_or_b32_e32 v3, v3, v1
	v_or_b32_e32 v4, v4, v130
	global_load_dwordx4 v[30:33], v3, s[46:47]
	global_load_dwordx4 v[34:37], v4, s[46:47]
	v_lshlrev_b32_sdwa v3, v198, v24 dst_sel:DWORD dst_unused:UNUSED_PAD src0_sel:DWORD src1_sel:WORD_1
	v_lshlrev_b32_sdwa v4, v198, v24 dst_sel:DWORD dst_unused:UNUSED_PAD src0_sel:DWORD src1_sel:WORD_0
	v_or_b32_e32 v3, v3, v1
	v_or_b32_e32 v4, v4, v130
	global_load_dwordx4 v[38:41], v3, s[46:47]
	global_load_dwordx4 v[42:45], v4, s[46:47]
	v_lshlrev_b32_sdwa v3, v198, v23 dst_sel:DWORD dst_unused:UNUSED_PAD src0_sel:DWORD src1_sel:WORD_1
	v_lshlrev_b32_sdwa v4, v198, v23 dst_sel:DWORD dst_unused:UNUSED_PAD src0_sel:DWORD src1_sel:WORD_0
	v_or_b32_e32 v3, v3, v1
	v_or_b32_e32 v4, v4, v130
	global_load_dwordx4 v[46:49], v3, s[46:47]
	global_load_dwordx4 v[50:53], v4, s[46:47]
	v_lshlrev_b32_sdwa v3, v198, v22 dst_sel:DWORD dst_unused:UNUSED_PAD src0_sel:DWORD src1_sel:WORD_1
	v_lshlrev_b32_sdwa v4, v198, v22 dst_sel:DWORD dst_unused:UNUSED_PAD src0_sel:DWORD src1_sel:WORD_0
	ds_read_b128 v[22:25], v2 offset:12288
	v_or_b32_e32 v3, v3, v1
	v_or_b32_e32 v4, v4, v130
	global_load_dwordx4 v[54:57], v3, s[46:47]
	global_load_dwordx4 v[58:61], v4, s[46:47]
	v_mov_b32_e32 v3, 0
	s_waitcnt vmcnt(15) lgkmcnt(0)
	v_dot4c_i32_i8_e32 v3, v22, v26
	v_dot4c_i32_i8_e32 v3, v23, v27
	v_mov_b32_e32 v27, 0
	s_waitcnt vmcnt(11)
	v_dot4c_i32_i8_e32 v27, v22, v74
	v_dot4c_i32_i8_e32 v27, v23, v75
	v_dot4c_i32_i8_e32 v3, v24, v28
	v_mov_b32_e32 v4, 0
	v_dot4c_i32_i8_e32 v27, v24, v76
	v_dot4c_i32_i8_e32 v3, v25, v29
	v_dot4c_i32_i8_e32 v4, v22, v62
	v_mov_b32_e32 v5, 0
	v_mov_b32_e32 v26, 0
	v_dot4c_i32_i8_e32 v27, v25, v77
	v_mov_b32_e32 v28, 0
	v_mov_b32_e32 v29, 0
	v_mov_b32_e32 v62, 0
	v_dot4c_i32_i8_e32 v5, v22, v66
	v_dot4c_i32_i8_e32 v26, v22, v70
	s_waitcnt vmcnt(10)
	v_dot4c_i32_i8_e32 v28, v22, v78
	s_waitcnt vmcnt(9)
	v_dot4c_i32_i8_e32 v29, v22, v82
	s_waitcnt vmcnt(8)
	v_dot4c_i32_i8_e32 v62, v22, v86
	v_cndmask_b32_e64 v22, v3, v27, s[2:3]
	v_dot4c_i32_i8_e32 v4, v23, v63
	v_dot4c_i32_i8_e32 v28, v23, v79
	ds_bpermute_b32 v22, v159, v22
	v_dot4c_i32_i8_e32 v4, v24, v64
	v_dot4c_i32_i8_e32 v28, v24, v80
	v_dot4c_i32_i8_e32 v4, v25, v65
	v_dot4c_i32_i8_e32 v5, v23, v67
	v_dot4c_i32_i8_e32 v28, v25, v81
	v_dot4c_i32_i8_e32 v29, v23, v83
	v_dot4c_i32_i8_e32 v5, v24, v68
	v_dot4c_i32_i8_e32 v26, v23, v71
	v_dot4c_i32_i8_e32 v29, v24, v84
	v_dot4c_i32_i8_e32 v62, v23, v87
	v_cndmask_b32_e64 v23, v4, v28, s[2:3]
	v_dot4c_i32_i8_e32 v5, v25, v69
	v_dot4c_i32_i8_e32 v29, v25, v85
	v_cndmask_b32_e64 v3, v27, v3, s[2:3]
	ds_bpermute_b32 v23, v159, v23
	s_waitcnt lgkmcnt(1)
	v_add_u32_e32 v3, v3, v22
	v_cndmask_b32_e64 v22, v5, v29, s[2:3]
	ds_bpermute_b32 v22, v159, v22
	v_dot4c_i32_i8_e32 v26, v24, v72
	v_dot4c_i32_i8_e32 v62, v24, v88
	v_dot4c_i32_i8_e32 v26, v25, v73
	v_dot4c_i32_i8_e32 v62, v25, v89
	v_cndmask_b32_e64 v4, v28, v4, s[2:3]
	s_waitcnt lgkmcnt(1)
	v_add_u32_e32 v4, v4, v23
	v_cndmask_b32_e64 v5, v29, v5, s[2:3]
	v_cndmask_b32_e64 v23, v26, v62, s[2:3]
	ds_bpermute_b32 v23, v159, v23
	s_waitcnt lgkmcnt(1)
	v_add_u32_e32 v5, v5, v22
	v_cndmask_b32_e64 v24, v3, v5, s[4:5]
	ds_bpermute_b32 v24, v160, v24
	v_cndmask_b32_e64 v22, v62, v26, s[2:3]
	s_waitcnt lgkmcnt(1)
	v_add_u32_e32 v22, v22, v23
	v_cndmask_b32_e64 v3, v5, v3, s[4:5]
	v_cndmask_b32_e64 v5, v4, v22, s[4:5]
	ds_bpermute_b32 v5, v160, v5
	s_waitcnt lgkmcnt(1)
	v_add_u32_e32 v3, v3, v24
	v_cndmask_b32_e64 v4, v22, v4, s[4:5]
	ds_read_b128 v[22:25], v181 offset:1920
	s_waitcnt lgkmcnt(1)
	v_add_u32_e32 v4, v4, v5
	v_cndmask_b32_e64 v5, v4, v3, s[6:7]
	v_cndmask_b32_e64 v3, v3, v4, s[6:7]
	ds_bpermute_b32 v3, v161, v3
	s_waitcnt lgkmcnt(1)
	v_lshlrev_b32_sdwa v4, v198, v22 dst_sel:DWORD dst_unused:UNUSED_PAD src0_sel:DWORD src1_sel:WORD_1
	v_lshlrev_b32_sdwa v22, v198, v22 dst_sel:DWORD dst_unused:UNUSED_PAD src0_sel:DWORD src1_sel:WORD_0
	v_or_b32_e32 v22, v22, v130
	v_or_b32_e32 v4, v4, v1
	global_load_dwordx4 v[26:29], v22, s[46:47]
	global_load_dwordx4 v[62:65], v4, s[46:47]
	v_lshlrev_b32_sdwa v22, v198, v23 dst_sel:DWORD dst_unused:UNUSED_PAD src0_sel:DWORD src1_sel:WORD_0
	v_lshlrev_b32_sdwa v4, v198, v23 dst_sel:DWORD dst_unused:UNUSED_PAD src0_sel:DWORD src1_sel:WORD_1
	v_or_b32_e32 v22, v22, v130
	v_or_b32_e32 v4, v4, v1
	global_load_dwordx4 v[66:69], v22, s[46:47]
	global_load_dwordx4 v[70:73], v4, s[46:47]
	v_lshlrev_b32_sdwa v22, v198, v24 dst_sel:DWORD dst_unused:UNUSED_PAD src0_sel:DWORD src1_sel:WORD_0
	v_lshlrev_b32_sdwa v4, v198, v24 dst_sel:DWORD dst_unused:UNUSED_PAD src0_sel:DWORD src1_sel:WORD_1
	v_or_b32_e32 v22, v22, v130
	v_or_b32_e32 v4, v4, v1
	global_load_dwordx4 v[74:77], v22, s[46:47]
	global_load_dwordx4 v[78:81], v4, s[46:47]
	v_lshlrev_b32_sdwa v82, v198, v25 dst_sel:DWORD dst_unused:UNUSED_PAD src0_sel:DWORD src1_sel:WORD_0
	v_lshlrev_b32_sdwa v4, v198, v25 dst_sel:DWORD dst_unused:UNUSED_PAD src0_sel:DWORD src1_sel:WORD_1
	v_or_b32_e32 v82, v82, v130
	v_or_b32_e32 v4, v4, v1
	ds_read_b128 v[22:25], v2 offset:14336
	global_load_dwordx4 v[82:85], v82, s[46:47]
	s_nop 0
	global_load_dwordx4 v[86:89], v4, s[46:47]
	v_mov_b32_e32 v4, 0
	s_waitcnt lgkmcnt(1)
	v_add3_u32 v19, v3, v19, v5
	s_waitcnt vmcnt(8) lgkmcnt(0)
	s_add_u32 s84, s37, s44
	s_addc_u32 s85, s39, s45
	s_cmpk_eq_i32 s44, 0x800
	ds_read_b128 v[216:219], v195
	s_waitcnt lgkmcnt(0)
; #define P9A_LOAD(W, J, H) do { _Pragma("unroll") for (int i = 0; i < 8; ++i) { const unsigned e = IDX16[(F.wave * 8 + (J)) * 128 + 64 * (H) + 8 * g + i]; W[i] = *(const GAS v4u*)(eb + (e * 2048u + lo)); } } while (0)
; DI void p9v2_phase(Frame& F) {
;     ...
;             P9A_LOAD(wA, 0, 0);
; #pragma unroll
;             for (int j = 0; j < 8; ++j) {
;                 P9A_LOAD(wB, j, 1);
;                 P9A_COMP(wA, j, 0);
;                 if (j < 7) P9A_LOAD(wA, j + 1, 0);
;                 P9A_COMP(wB, j, 1);
;             }
;     ...
;         }
	v_lshlrev_b32_sdwa v214, v198, v216 dst_sel:DWORD dst_unused:UNUSED_PAD src0_sel:DWORD src1_sel:WORD_0
	v_lshlrev_b32_sdwa v215, v198, v216 dst_sel:DWORD dst_unused:UNUSED_PAD src0_sel:DWORD src1_sel:WORD_1
	v_or_b32_e32 v214, v214, v130
	v_or_b32_e32 v215, v215, v1
	global_load_dwordx4 v[220:223], v214, s[84:85]
	global_load_dwordx4 v[224:227], v215, s[84:85]
	v_lshlrev_b32_sdwa v214, v198, v217 dst_sel:DWORD dst_unused:UNUSED_PAD src0_sel:DWORD src1_sel:WORD_0
	v_lshlrev_b32_sdwa v215, v198, v217 dst_sel:DWORD dst_unused:UNUSED_PAD src0_sel:DWORD src1_sel:WORD_1
	v_or_b32_e32 v214, v214, v130
	v_or_b32_e32 v215, v215, v1
	global_load_dwordx4 v[228:231], v214, s[84:85]
	global_load_dwordx4 v[232:235], v215, s[84:85]
	v_lshlrev_b32_sdwa v214, v198, v218 dst_sel:DWORD dst_unused:UNUSED_PAD src0_sel:DWORD src1_sel:WORD_0
	v_lshlrev_b32_sdwa v215, v198, v218 dst_sel:DWORD dst_unused:UNUSED_PAD src0_sel:DWORD src1_sel:WORD_1
	v_or_b32_e32 v214, v214, v130
	v_or_b32_e32 v215, v215, v1
	global_load_dwordx4 v[236:239], v214, s[84:85]
	global_load_dwordx4 v[240:243], v215, s[84:85]
	v_lshlrev_b32_sdwa v214, v198, v219 dst_sel:DWORD dst_unused:UNUSED_PAD src0_sel:DWORD src1_sel:WORD_0
	v_lshlrev_b32_sdwa v215, v198, v219 dst_sel:DWORD dst_unused:UNUSED_PAD src0_sel:DWORD src1_sel:WORD_1
	v_or_b32_e32 v214, v214, v130
	v_or_b32_e32 v215, v215, v1
	global_load_dwordx4 v[244:247], v214, s[84:85]
	global_load_dwordx4 v[248:251], v215, s[84:85]
	v_dot4c_i32_i8_e32 v4, v22, v58
	v_mov_b32_e32 v58, 0
	v_dot4c_i32_i8_e32 v58, v22, v54
	v_mov_b32_e32 v54, 0
	v_dot4c_i32_i8_e32 v54, v22, v50
	v_mov_b32_e32 v50, 0
	v_dot4c_i32_i8_e32 v50, v22, v46
	v_mov_b32_e32 v46, 0
	v_dot4c_i32_i8_e32 v46, v22, v42
	v_mov_b32_e32 v42, 0
	v_dot4c_i32_i8_e32 v4, v23, v59
	v_dot4c_i32_i8_e32 v46, v23, v43
	v_dot4c_i32_i8_e32 v42, v22, v38
	v_dot4c_i32_i8_e32 v4, v24, v60
	v_dot4c_i32_i8_e32 v58, v23, v55
	v_dot4c_i32_i8_e32 v46, v24, v44
	v_dot4c_i32_i8_e32 v42, v23, v39
	v_mov_b32_e32 v38, 0
	v_dot4c_i32_i8_e32 v4, v25, v61
	v_dot4c_i32_i8_e32 v58, v24, v56
	v_dot4c_i32_i8_e32 v46, v25, v45
	v_dot4c_i32_i8_e32 v42, v24, v40
	v_dot4c_i32_i8_e32 v38, v22, v34
	v_mov_b32_e32 v34, 0
	v_dot4c_i32_i8_e32 v58, v25, v57
	v_dot4c_i32_i8_e32 v54, v23, v51
	v_dot4c_i32_i8_e32 v42, v25, v41
	v_dot4c_i32_i8_e32 v38, v23, v35
	v_dot4c_i32_i8_e32 v34, v22, v30
	v_cndmask_b32_e64 v22, v4, v46, s[2:3]
	v_dot4c_i32_i8_e32 v54, v24, v52
	v_dot4c_i32_i8_e32 v50, v23, v47
	v_dot4c_i32_i8_e32 v38, v24, v36
	v_dot4c_i32_i8_e32 v34, v23, v31
	ds_bpermute_b32 v22, v159, v22
	v_cndmask_b32_e64 v23, v58, v42, s[2:3]
	v_dot4c_i32_i8_e32 v54, v25, v53
	v_dot4c_i32_i8_e32 v38, v25, v37
	ds_bpermute_b32 v23, v159, v23
	v_dot4c_i32_i8_e32 v50, v24, v48
	v_dot4c_i32_i8_e32 v34, v24, v32
	v_cndmask_b32_e64 v24, v54, v38, s[2:3]
	ds_bpermute_b32 v24, v159, v24
	v_cndmask_b32_e64 v4, v46, v4, s[2:3]
	v_dot4c_i32_i8_e32 v50, v25, v49
	v_dot4c_i32_i8_e32 v34, v25, v33
	s_waitcnt lgkmcnt(2)
	v_add_u32_e32 v4, v4, v22
	v_cndmask_b32_e64 v22, v42, v58, s[2:3]
	s_waitcnt lgkmcnt(1)
	v_add_u32_e32 v30, v22, v23
	v_cndmask_b32_e64 v23, v50, v34, s[2:3]
	v_cndmask_b32_e64 v22, v38, v54, s[2:3]
	ds_bpermute_b32 v23, v159, v23
	s_waitcnt lgkmcnt(1)
	v_add_u32_e32 v22, v22, v24
	v_cndmask_b32_e64 v25, v4, v22, s[4:5]
	ds_bpermute_b32 v25, v160, v25
	v_cndmask_b32_e64 v24, v34, v50, s[2:3]
	s_waitcnt lgkmcnt(1)
	v_add_u32_e32 v31, v24, v23
	v_cndmask_b32_e64 v4, v22, v4, s[4:5]
	v_cndmask_b32_e64 v22, v30, v31, s[4:5]
	ds_bpermute_b32 v32, v160, v22
	s_waitcnt lgkmcnt(1)
	v_add_u32_e32 v4, v4, v25
	ds_read_b128 v[22:25], v2 offset:14336
	v_cndmask_b32_e64 v30, v31, v30, s[4:5]
	v_mov_b32_e32 v33, 0
	s_waitcnt lgkmcnt(1)
	v_add_u32_e32 v30, v30, v32
	v_mov_b32_e32 v32, 0
	s_waitcnt vmcnt(15) lgkmcnt(0)
	v_dot4c_i32_i8_e32 v32, v22, v26
	v_dot4c_i32_i8_e32 v32, v23, v27
	v_dot4c_i32_i8_e32 v32, v24, v28
	v_dot4c_i32_i8_e32 v32, v25, v29
	v_mov_b32_e32 v29, 0
	s_waitcnt vmcnt(11)
	v_dot4c_i32_i8_e32 v29, v22, v74
	v_dot4c_i32_i8_e32 v29, v23, v75
	v_dot4c_i32_i8_e32 v29, v24, v76
	v_mov_b32_e32 v26, 0
	v_mov_b32_e32 v27, 0
	v_mov_b32_e32 v28, 0
	v_dot4c_i32_i8_e32 v29, v25, v77
	v_mov_b32_e32 v34, 0
	v_mov_b32_e32 v35, 0
	v_dot4c_i32_i8_e32 v26, v22, v62
	v_dot4c_i32_i8_e32 v27, v22, v66
	v_dot4c_i32_i8_e32 v28, v22, v70
	s_waitcnt vmcnt(10)
	v_dot4c_i32_i8_e32 v33, v22, v78
	s_waitcnt vmcnt(9)
	v_dot4c_i32_i8_e32 v34, v22, v82
	s_waitcnt vmcnt(8)
	v_dot4c_i32_i8_e32 v35, v22, v86
	v_cndmask_b32_e64 v22, v32, v29, s[2:3]
	v_dot4c_i32_i8_e32 v26, v23, v63
	v_dot4c_i32_i8_e32 v33, v23, v79
	ds_bpermute_b32 v22, v159, v22
	v_dot4c_i32_i8_e32 v26, v24, v64
	v_dot4c_i32_i8_e32 v27, v23, v67
	v_dot4c_i32_i8_e32 v33, v24, v80
	v_dot4c_i32_i8_e32 v34, v23, v83
	v_dot4c_i32_i8_e32 v26, v25, v65
	v_dot4c_i32_i8_e32 v27, v24, v68
	v_dot4c_i32_i8_e32 v28, v23, v71
	v_dot4c_i32_i8_e32 v33, v25, v81
	v_dot4c_i32_i8_e32 v34, v24, v84
	v_dot4c_i32_i8_e32 v35, v23, v87
	v_dot4c_i32_i8_e32 v27, v25, v69
	v_dot4c_i32_i8_e32 v28, v24, v72
	v_dot4c_i32_i8_e32 v34, v25, v85
	v_dot4c_i32_i8_e32 v35, v24, v88
	v_cndmask_b32_e64 v24, v26, v33, s[2:3]
	v_dot4c_i32_i8_e32 v28, v25, v73
	v_dot4c_i32_i8_e32 v35, v25, v89
	v_cndmask_b32_e64 v23, v29, v32, s[2:3]
	ds_bpermute_b32 v24, v159, v24
	v_cndmask_b32_e64 v25, v27, v34, s[2:3]
	s_waitcnt lgkmcnt(1)
	v_add_u32_e32 v22, v23, v22
	v_cndmask_b32_e64 v23, v33, v26, s[2:3]
	ds_bpermute_b32 v25, v159, v25
	v_cndmask_b32_e64 v26, v28, v35, s[2:3]
	ds_bpermute_b32 v26, v159, v26
	s_waitcnt lgkmcnt(2)
	v_add_u32_e32 v23, v23, v24
	v_cndmask_b32_e64 v24, v34, v27, s[2:3]
	s_waitcnt lgkmcnt(1)
	v_add_u32_e32 v24, v24, v25
	v_cndmask_b32_e64 v25, v35, v28, s[2:3]
	s_waitcnt lgkmcnt(0)
	v_add_u32_e32 v25, v25, v26
	v_cndmask_b32_e64 v26, v22, v24, s[4:5]
	v_cndmask_b32_e64 v27, v23, v25, s[4:5]
	ds_bpermute_b32 v26, v160, v26
	ds_bpermute_b32 v27, v160, v27
	v_cndmask_b32_e64 v22, v24, v22, s[4:5]
	v_cndmask_b32_e64 v23, v25, v23, s[4:5]
	v_cndmask_b32_e64 v31, v4, v30, s[6:7]
	s_waitcnt lgkmcnt(1)
	v_add_u32_e32 v22, v22, v26
	s_waitcnt lgkmcnt(0)
	v_add_u32_e32 v23, v23, v27
	ds_bpermute_b32 v28, v161, v31
	v_cndmask_b32_e64 v24, v22, v23, s[6:7]
	ds_bpermute_b32 v24, v161, v24
	v_cndmask_b32_e64 v3, v30, v4, s[6:7]
	s_waitcnt lgkmcnt(1)
	v_add3_u32 v20, v28, v20, v3
	v_cndmask_b32_e64 v3, v23, v22, s[6:7]
	s_waitcnt lgkmcnt(0)
	v_add3_u32 v21, v24, v21, v3
	v_add_u32_e32 v2, 0x80, v2
	s_cbranch_scc1 .LBB0_1307
